# XCD-contiguous MoE order + in five GEMM K-loops (P1, P7, P8, P9, P14): static priority 1 for waves 4-7 (per-segment flips deleted) and LDS-DMA issue ahead of the ds_reads in each load segment
# baseline (speedup 1.0000x reference)
.Lsp130:
.LBB0_130:
	s_add_u32 s4, s38, 0x80
	s_addc_u32 s5, s39, 0
	s_add_i32 s31, 0, 0x10000
	s_cmp_eq_u32 s29, 28
	s_cselect_b32 s5, s35, s5
	s_cselect_b32 s4, s34, s4
	s_cselect_b32 s43, s37, s15
	s_cselect_b32 s42, s36, s14
	s_add_i32 s68, 0, 0x14000
	v_lshl_add_u64 v[146:147], s[38:39], 0, v[144:145]
	s_add_i32 m0, s48, 0xc000
	s_nop 0
	global_load_lds_dwordx4 v[146:147], off
	v_lshl_add_u64 v[146:147], s[38:39], 0, v[142:143]
	s_add_i32 m0, s48, 0xe000
	s_nop 0
	global_load_lds_dwordx4 v[146:147], off
	v_add_u32_e32 v146, s31, v148
	ds_read_b128 v[152:155], v146
	ds_read_b128 v[156:159], v146 offset:1024
	ds_read_b128 v[160:163], v146 offset:2048
	ds_read_b128 v[164:167], v146 offset:3072
	v_add_u32_e32 v146, s68, v148
	ds_read_b128 v[168:171], v146
	ds_read_b128 v[172:175], v146 offset:1024
	ds_read_b128 v[176:179], v146 offset:2048
	ds_read_b128 v[180:183], v146 offset:3072
	ds_read_b128 v[184:187], v150
	ds_read_b128 v[188:191], v150 offset:1024
	ds_read_b128 v[192:195], v150 offset:2048
	ds_read_b128 v[196:199], v150 offset:3072
	ds_read_b128 v[224:227], v150 offset:4096
	ds_read_b128 v[228:231], v150 offset:5120
	ds_read_b128 v[238:241], v150 offset:6144
	ds_read_b128 v[242:245], v150 offset:7168
	s_waitcnt vmcnt(8)
	s_waitcnt lgkmcnt(0)
	s_barrier
	s_waitcnt lgkmcnt(0)
	v_mfma_f32_16x16x32_bf16 v[128:131], v[152:155], v[184:187], v[128:131]
	v_mfma_f32_16x16x32_bf16 v[124:127], v[160:163], v[184:187], v[124:127]
	v_mfma_f32_16x16x32_bf16 v[120:123], v[152:155], v[192:195], v[120:123]
	v_mfma_f32_16x16x32_bf16 v[112:115], v[160:163], v[192:195], v[112:115]
	v_mfma_f32_16x16x32_bf16 v[104:107], v[152:155], v[224:227], v[104:107]
	v_mfma_f32_16x16x32_bf16 v[96:99], v[160:163], v[224:227], v[96:99]
	v_mfma_f32_16x16x32_bf16 v[88:91], v[152:155], v[238:241], v[88:91]
	v_mfma_f32_16x16x32_bf16 v[80:83], v[160:163], v[238:241], v[80:83]
	v_mfma_f32_16x16x32_bf16 v[128:131], v[156:159], v[188:191], v[128:131]
	v_mfma_f32_16x16x32_bf16 v[124:127], v[164:167], v[188:191], v[124:127]
	v_mfma_f32_16x16x32_bf16 v[120:123], v[156:159], v[196:199], v[120:123]
	v_mfma_f32_16x16x32_bf16 v[112:115], v[164:167], v[196:199], v[112:115]
	v_mfma_f32_16x16x32_bf16 v[104:107], v[156:159], v[228:231], v[104:107]
	v_mfma_f32_16x16x32_bf16 v[96:99], v[164:167], v[228:231], v[96:99]
	v_mfma_f32_16x16x32_bf16 v[88:91], v[156:159], v[242:245], v[88:91]
	v_mfma_f32_16x16x32_bf16 v[80:83], v[164:167], v[242:245], v[80:83]
	v_mfma_f32_16x16x32_bf16 v[116:119], v[168:171], v[184:187], v[116:119]
	v_mfma_f32_16x16x32_bf16 v[108:111], v[176:179], v[184:187], v[108:111]
	v_mfma_f32_16x16x32_bf16 v[100:103], v[168:171], v[192:195], v[100:103]
	v_mfma_f32_16x16x32_bf16 v[92:95], v[176:179], v[192:195], v[92:95]
	v_mfma_f32_16x16x32_bf16 v[84:87], v[168:171], v[224:227], v[84:87]
	v_mfma_f32_16x16x32_bf16 v[76:79], v[176:179], v[224:227], v[76:79]
	v_mfma_f32_16x16x32_bf16 v[72:75], v[168:171], v[238:241], v[72:75]
	v_mfma_f32_16x16x32_bf16 v[68:71], v[176:179], v[238:241], v[68:71]
	v_mfma_f32_16x16x32_bf16 v[116:119], v[172:175], v[188:191], v[116:119]
	v_mfma_f32_16x16x32_bf16 v[108:111], v[180:183], v[188:191], v[108:111]
	v_mfma_f32_16x16x32_bf16 v[100:103], v[172:175], v[196:199], v[100:103]
	v_mfma_f32_16x16x32_bf16 v[92:95], v[180:183], v[196:199], v[92:95]
	v_mfma_f32_16x16x32_bf16 v[84:87], v[172:175], v[228:231], v[84:87]
	v_mfma_f32_16x16x32_bf16 v[76:79], v[180:183], v[228:231], v[76:79]
	v_mfma_f32_16x16x32_bf16 v[72:75], v[172:175], v[242:245], v[72:75]
	v_mfma_f32_16x16x32_bf16 v[68:71], v[180:183], v[242:245], v[68:71]
	s_barrier
	s_add_i32 s31, s31, s47
	v_lshl_add_u64 v[146:147], s[42:43], 0, v[34:35]
	s_mov_b32 m0, s31
	s_nop 0
	global_load_lds_dwordx4 v[146:147], off
	s_add_i32 m0, s31, 0x2000
	s_add_u32 s64, s42, 0x80000
	v_lshl_add_u64 v[212:213], s[42:43], 0, v[132:133]
	s_addc_u32 s65, s43, 0
	s_add_i32 s31, s68, s47
	global_load_lds_dwordx4 v[212:213], off
	v_lshl_add_u64 v[232:233], s[64:65], 0, v[34:35]
	s_mov_b32 m0, s31
	v_lshl_add_u64 v[246:247], s[4:5], 0, v[134:135]
	global_load_lds_dwordx4 v[232:233], off
	v_lshl_add_u64 v[232:233], s[64:65], 0, v[132:133]
	s_add_i32 m0, s31, 0x2000
	s_nop 0
	global_load_lds_dwordx4 v[232:233], off
	v_lshl_add_u64 v[232:233], s[4:5], 0, v[138:139]
	s_mov_b32 m0, s48
	s_nop 0
	global_load_lds_dwordx4 v[232:233], off
	s_mov_b32 m0, s49
	s_nop 0
	global_load_lds_dwordx4 v[246:247], off
	ds_read_b128 v[184:187], v150 offset:16384
	ds_read_b128 v[188:191], v150 offset:17408
	ds_read_b128 v[192:195], v150 offset:18432
	ds_read_b128 v[196:199], v150 offset:19456
	ds_read_b128 v[224:227], v150 offset:20480
	ds_read_b128 v[228:231], v150 offset:21504
	ds_read_b128 v[238:241], v150 offset:22528
	ds_read_b128 v[242:245], v150 offset:23552
	s_waitcnt vmcnt(8)
	s_waitcnt lgkmcnt(0)
	s_barrier
	s_waitcnt lgkmcnt(0)
	v_mfma_f32_16x16x32_bf16 v[64:67], v[152:155], v[184:187], v[64:67]
	v_mfma_f32_16x16x32_bf16 v[60:63], v[160:163], v[184:187], v[60:63]
	v_mfma_f32_16x16x32_bf16 v[52:55], v[152:155], v[192:195], v[52:55]
	v_mfma_f32_16x16x32_bf16 v[44:47], v[160:163], v[192:195], v[44:47]
	v_mfma_f32_16x16x32_bf16 v[36:39], v[152:155], v[224:227], v[36:39]
	v_mfma_f32_16x16x32_bf16 v[26:29], v[160:163], v[224:227], v[26:29]
	v_mfma_f32_16x16x32_bf16 v[18:21], v[152:155], v[238:241], v[18:21]
	v_mfma_f32_16x16x32_bf16 v[10:13], v[160:163], v[238:241], v[10:13]
	v_mfma_f32_16x16x32_bf16 v[64:67], v[156:159], v[188:191], v[64:67]
	v_mfma_f32_16x16x32_bf16 v[60:63], v[164:167], v[188:191], v[60:63]
	v_mfma_f32_16x16x32_bf16 v[52:55], v[156:159], v[196:199], v[52:55]
	v_mfma_f32_16x16x32_bf16 v[44:47], v[164:167], v[196:199], v[44:47]
	v_mfma_f32_16x16x32_bf16 v[36:39], v[156:159], v[228:231], v[36:39]
	v_mfma_f32_16x16x32_bf16 v[26:29], v[164:167], v[228:231], v[26:29]
	v_mfma_f32_16x16x32_bf16 v[18:21], v[156:159], v[242:245], v[18:21]
	v_mfma_f32_16x16x32_bf16 v[10:13], v[164:167], v[242:245], v[10:13]
	v_mfma_f32_16x16x32_bf16 v[56:59], v[168:171], v[184:187], v[56:59]
	v_mfma_f32_16x16x32_bf16 v[48:51], v[176:179], v[184:187], v[48:51]
	v_mfma_f32_16x16x32_bf16 v[40:43], v[168:171], v[192:195], v[40:43]
	v_mfma_f32_16x16x32_bf16 v[30:33], v[176:179], v[192:195], v[30:33]
	v_mfma_f32_16x16x32_bf16 v[22:25], v[168:171], v[224:227], v[22:25]
	v_mfma_f32_16x16x32_bf16 v[14:17], v[176:179], v[224:227], v[14:17]
	v_mfma_f32_16x16x32_bf16 v[6:9], v[168:171], v[238:241], v[6:9]
	v_mfma_f32_16x16x32_bf16 v[2:5], v[176:179], v[238:241], v[2:5]
	v_mfma_f32_16x16x32_bf16 v[56:59], v[172:175], v[188:191], v[56:59]
	v_mfma_f32_16x16x32_bf16 v[48:51], v[180:183], v[188:191], v[48:51]
	v_mfma_f32_16x16x32_bf16 v[40:43], v[172:175], v[196:199], v[40:43]
	v_mfma_f32_16x16x32_bf16 v[30:33], v[180:183], v[196:199], v[30:33]
	v_mfma_f32_16x16x32_bf16 v[22:25], v[172:175], v[228:231], v[22:25]
	v_mfma_f32_16x16x32_bf16 v[14:17], v[180:183], v[228:231], v[14:17]
	v_mfma_f32_16x16x32_bf16 v[6:9], v[172:175], v[242:245], v[6:9]
	v_mfma_f32_16x16x32_bf16 v[2:5], v[180:183], v[242:245], v[2:5]
	s_barrier
	s_add_i32 s31, 0, 0x18000
	s_add_i32 s64, 0, 0x1c000
	s_mov_b32 m0, s50
	v_lshl_add_u64 v[248:249], s[4:5], 0, v[140:141]
	global_load_lds_dwordx4 v[248:249], off
	v_lshl_add_u64 v[248:249], s[4:5], 0, v[136:137]
	s_mov_b32 m0, s51
	s_nop 0
	global_load_lds_dwordx4 v[248:249], off
	v_add_u32_e32 v151, s31, v148
	ds_read_b128 v[152:155], v151
	ds_read_b128 v[156:159], v151 offset:1024
	ds_read_b128 v[160:163], v151 offset:2048
	ds_read_b128 v[164:167], v151 offset:3072
	v_add_u32_e32 v151, s64, v148
	ds_read_b128 v[168:171], v151
	ds_read_b128 v[172:175], v151 offset:1024
	ds_read_b128 v[176:179], v151 offset:2048
	ds_read_b128 v[180:183], v151 offset:3072
	ds_read_b128 v[184:187], v150 offset:32768
	ds_read_b128 v[188:191], v150 offset:33792
	ds_read_b128 v[192:195], v150 offset:34816
	ds_read_b128 v[196:199], v150 offset:35840
	ds_read_b128 v[224:227], v150 offset:36864
	ds_read_b128 v[228:231], v150 offset:37888
	ds_read_b128 v[238:241], v150 offset:38912
	ds_read_b128 v[242:245], v150 offset:39936
	s_waitcnt vmcnt(8)
	s_waitcnt lgkmcnt(0)
	s_barrier
	s_waitcnt lgkmcnt(0)
	v_mfma_f32_16x16x32_bf16 v[128:131], v[152:155], v[184:187], v[128:131]
	v_mfma_f32_16x16x32_bf16 v[124:127], v[160:163], v[184:187], v[124:127]
	v_mfma_f32_16x16x32_bf16 v[120:123], v[152:155], v[192:195], v[120:123]
	v_mfma_f32_16x16x32_bf16 v[112:115], v[160:163], v[192:195], v[112:115]
	v_mfma_f32_16x16x32_bf16 v[104:107], v[152:155], v[224:227], v[104:107]
	v_mfma_f32_16x16x32_bf16 v[96:99], v[160:163], v[224:227], v[96:99]
	v_mfma_f32_16x16x32_bf16 v[88:91], v[152:155], v[238:241], v[88:91]
	v_mfma_f32_16x16x32_bf16 v[80:83], v[160:163], v[238:241], v[80:83]
	v_mfma_f32_16x16x32_bf16 v[128:131], v[156:159], v[188:191], v[128:131]
	v_mfma_f32_16x16x32_bf16 v[124:127], v[164:167], v[188:191], v[124:127]
	v_mfma_f32_16x16x32_bf16 v[120:123], v[156:159], v[196:199], v[120:123]
	v_mfma_f32_16x16x32_bf16 v[112:115], v[164:167], v[196:199], v[112:115]
	v_mfma_f32_16x16x32_bf16 v[104:107], v[156:159], v[228:231], v[104:107]
	v_mfma_f32_16x16x32_bf16 v[96:99], v[164:167], v[228:231], v[96:99]
	v_mfma_f32_16x16x32_bf16 v[88:91], v[156:159], v[242:245], v[88:91]
	v_mfma_f32_16x16x32_bf16 v[80:83], v[164:167], v[242:245], v[80:83]
	v_mfma_f32_16x16x32_bf16 v[116:119], v[168:171], v[184:187], v[116:119]
	v_mfma_f32_16x16x32_bf16 v[108:111], v[176:179], v[184:187], v[108:111]
	v_mfma_f32_16x16x32_bf16 v[100:103], v[168:171], v[192:195], v[100:103]
	v_mfma_f32_16x16x32_bf16 v[92:95], v[176:179], v[192:195], v[92:95]
	v_mfma_f32_16x16x32_bf16 v[84:87], v[168:171], v[224:227], v[84:87]
	v_mfma_f32_16x16x32_bf16 v[76:79], v[176:179], v[224:227], v[76:79]
	v_mfma_f32_16x16x32_bf16 v[72:75], v[168:171], v[238:241], v[72:75]
	v_mfma_f32_16x16x32_bf16 v[68:71], v[176:179], v[238:241], v[68:71]
	v_mfma_f32_16x16x32_bf16 v[116:119], v[172:175], v[188:191], v[116:119]
	v_mfma_f32_16x16x32_bf16 v[108:111], v[180:183], v[188:191], v[108:111]
	v_mfma_f32_16x16x32_bf16 v[100:103], v[172:175], v[196:199], v[100:103]
	v_mfma_f32_16x16x32_bf16 v[92:95], v[180:183], v[196:199], v[92:95]
	v_mfma_f32_16x16x32_bf16 v[84:87], v[172:175], v[228:231], v[84:87]
	v_mfma_f32_16x16x32_bf16 v[76:79], v[180:183], v[228:231], v[76:79]
	v_mfma_f32_16x16x32_bf16 v[72:75], v[172:175], v[242:245], v[72:75]
	v_mfma_f32_16x16x32_bf16 v[68:71], v[180:183], v[242:245], v[68:71]
	s_barrier
	s_add_i32 s4, s31, s47
	v_lshl_add_u64 v[146:147], v[146:147], 0, s[78:79]
	s_mov_b32 m0, s4
	s_nop 0
	global_load_lds_dwordx4 v[146:147], off
	s_add_i32 m0, s4, 0x2000
	s_add_u32 s4, s42, 0x80080
	v_lshl_add_u64 v[146:147], v[212:213], 0, s[78:79]
	s_addc_u32 s5, s43, 0
	s_add_i32 s31, s64, s47
	global_load_lds_dwordx4 v[146:147], off
	v_lshl_add_u64 v[146:147], s[4:5], 0, v[34:35]
	s_mov_b32 m0, s31
	s_nop 0
	global_load_lds_dwordx4 v[146:147], off
	v_lshl_add_u64 v[146:147], s[4:5], 0, v[132:133]
	s_add_i32 m0, s31, 0x2000
	s_nop 0
	global_load_lds_dwordx4 v[146:147], off
	v_lshl_add_u64 v[146:147], v[232:233], 0, s[78:79]
	s_mov_b32 m0, s52
	s_nop 0
	global_load_lds_dwordx4 v[146:147], off
	v_lshl_add_u64 v[146:147], v[246:247], 0, s[78:79]
	s_mov_b32 m0, s53
	s_nop 0
	global_load_lds_dwordx4 v[146:147], off
	ds_read_b128 v[184:187], v150 offset:49152
	ds_read_b128 v[188:191], v150 offset:50176
	ds_read_b128 v[192:195], v150 offset:51200
	ds_read_b128 v[196:199], v150 offset:52224
	ds_read_b128 v[224:227], v150 offset:53248
	ds_read_b128 v[228:231], v150 offset:54272
	ds_read_b128 v[238:241], v150 offset:55296
	ds_read_b128 v[242:245], v150 offset:56320
	s_waitcnt vmcnt(8)
	s_waitcnt lgkmcnt(0)
	s_barrier
	s_waitcnt lgkmcnt(0)
	v_mfma_f32_16x16x32_bf16 v[64:67], v[152:155], v[184:187], v[64:67]
	v_mfma_f32_16x16x32_bf16 v[60:63], v[160:163], v[184:187], v[60:63]
	v_mfma_f32_16x16x32_bf16 v[52:55], v[152:155], v[192:195], v[52:55]
	v_mfma_f32_16x16x32_bf16 v[44:47], v[160:163], v[192:195], v[44:47]
	v_mfma_f32_16x16x32_bf16 v[36:39], v[152:155], v[224:227], v[36:39]
	v_mfma_f32_16x16x32_bf16 v[26:29], v[160:163], v[224:227], v[26:29]
	v_mfma_f32_16x16x32_bf16 v[18:21], v[152:155], v[238:241], v[18:21]
	v_mfma_f32_16x16x32_bf16 v[10:13], v[160:163], v[238:241], v[10:13]
	v_mfma_f32_16x16x32_bf16 v[64:67], v[156:159], v[188:191], v[64:67]
	v_mfma_f32_16x16x32_bf16 v[60:63], v[164:167], v[188:191], v[60:63]
	v_mfma_f32_16x16x32_bf16 v[52:55], v[156:159], v[196:199], v[52:55]
	v_mfma_f32_16x16x32_bf16 v[44:47], v[164:167], v[196:199], v[44:47]
	v_mfma_f32_16x16x32_bf16 v[36:39], v[156:159], v[228:231], v[36:39]
	v_mfma_f32_16x16x32_bf16 v[26:29], v[164:167], v[228:231], v[26:29]
	v_mfma_f32_16x16x32_bf16 v[18:21], v[156:159], v[242:245], v[18:21]
	v_mfma_f32_16x16x32_bf16 v[10:13], v[164:167], v[242:245], v[10:13]
	v_mfma_f32_16x16x32_bf16 v[56:59], v[168:171], v[184:187], v[56:59]
	v_mfma_f32_16x16x32_bf16 v[48:51], v[176:179], v[184:187], v[48:51]
	v_mfma_f32_16x16x32_bf16 v[40:43], v[168:171], v[192:195], v[40:43]
	v_mfma_f32_16x16x32_bf16 v[30:33], v[176:179], v[192:195], v[30:33]
	v_mfma_f32_16x16x32_bf16 v[22:25], v[168:171], v[224:227], v[22:25]
	v_mfma_f32_16x16x32_bf16 v[14:17], v[176:179], v[224:227], v[14:17]
	v_mfma_f32_16x16x32_bf16 v[6:9], v[168:171], v[238:241], v[6:9]
	v_mfma_f32_16x16x32_bf16 v[2:5], v[176:179], v[238:241], v[2:5]
	v_mfma_f32_16x16x32_bf16 v[56:59], v[172:175], v[188:191], v[56:59]
	v_mfma_f32_16x16x32_bf16 v[48:51], v[180:183], v[188:191], v[48:51]
	v_mfma_f32_16x16x32_bf16 v[40:43], v[172:175], v[196:199], v[40:43]
	v_mfma_f32_16x16x32_bf16 v[30:33], v[180:183], v[196:199], v[30:33]
	v_mfma_f32_16x16x32_bf16 v[22:25], v[172:175], v[228:231], v[22:25]
	v_mfma_f32_16x16x32_bf16 v[14:17], v[180:183], v[228:231], v[14:17]
	v_mfma_f32_16x16x32_bf16 v[6:9], v[172:175], v[242:245], v[6:9]
	v_mfma_f32_16x16x32_bf16 v[2:5], v[180:183], v[242:245], v[2:5]
	s_barrier
	s_add_i32 s29, s29, 2
	s_add_u32 s14, s14, 0x100
	s_addc_u32 s15, s15, 0
	s_add_u32 s38, s38, 0x100
	s_addc_u32 s39, s39, 0
	s_cmp_gt_u32 s29, 29
	s_cbranch_scc0 .LBB0_130
	s_setprio 0
	s_and_b64 vcc, exec, s[22:23]
	s_cbranch_vccz .LBB0_133
	s_barrier

.Lsp607:
.LBB0_607:
	s_add_u32 s4, s30, 0x80
	s_addc_u32 s5, s31, 0
	s_add_i32 s53, 0, 0x10000
	s_cmp_eq_u32 s52, 28
	s_cselect_b32 s5, s27, s5
	s_cselect_b32 s4, s26, s4
	s_cselect_b32 s35, s29, s25
	s_cselect_b32 s34, s28, s23
	s_add_i32 s56, 0, 0x14000
	v_lshl_add_u64 v[198:199], s[30:31], 0, v[144:145]
	s_add_i32 m0, s42, 0xc000
	s_nop 0
	global_load_lds_dwordx4 v[198:199], off
	v_lshl_add_u64 v[198:199], s[30:31], 0, v[142:143]
	s_add_i32 m0, s42, 0xe000
	s_nop 0
	global_load_lds_dwordx4 v[198:199], off
	v_add_u32_e32 v153, s53, v150
	ds_read_b128 v[146:149], v153
	ds_read_b128 v[154:157], v153 offset:1024
	ds_read_b128 v[158:161], v153 offset:2048
	ds_read_b128 v[162:165], v153 offset:3072
	v_add_u32_e32 v153, s56, v150
	ds_read_b128 v[166:169], v153
	ds_read_b128 v[170:173], v153 offset:1024
	ds_read_b128 v[174:177], v153 offset:2048
	ds_read_b128 v[178:181], v153 offset:3072
	ds_read_b128 v[182:185], v152
	ds_read_b128 v[186:189], v152 offset:1024
	ds_read_b128 v[190:193], v152 offset:2048
	ds_read_b128 v[194:197], v152 offset:3072
	ds_read_b128 v[224:227], v152 offset:4096
	ds_read_b128 v[228:231], v152 offset:5120
	ds_read_b128 v[238:241], v152 offset:6144
	ds_read_b128 v[242:245], v152 offset:7168
	s_waitcnt vmcnt(8)
	s_waitcnt lgkmcnt(0)
	s_barrier
	s_waitcnt lgkmcnt(0)
	v_mfma_f32_16x16x32_bf16 v[128:131], v[146:149], v[182:185], v[128:131]
	v_mfma_f32_16x16x32_bf16 v[124:127], v[158:161], v[182:185], v[124:127]
	v_mfma_f32_16x16x32_bf16 v[112:115], v[146:149], v[190:193], v[112:115]
	v_mfma_f32_16x16x32_bf16 v[108:111], v[158:161], v[190:193], v[108:111]
	v_mfma_f32_16x16x32_bf16 v[96:99], v[146:149], v[224:227], v[96:99]
	v_mfma_f32_16x16x32_bf16 v[92:95], v[158:161], v[224:227], v[92:95]
	v_mfma_f32_16x16x32_bf16 v[80:83], v[146:149], v[238:241], v[80:83]
	v_mfma_f32_16x16x32_bf16 v[76:79], v[158:161], v[238:241], v[76:79]
	v_mfma_f32_16x16x32_bf16 v[128:131], v[154:157], v[186:189], v[128:131]
	v_mfma_f32_16x16x32_bf16 v[124:127], v[162:165], v[186:189], v[124:127]
	v_mfma_f32_16x16x32_bf16 v[112:115], v[154:157], v[194:197], v[112:115]
	v_mfma_f32_16x16x32_bf16 v[108:111], v[162:165], v[194:197], v[108:111]
	v_mfma_f32_16x16x32_bf16 v[96:99], v[154:157], v[228:231], v[96:99]
	v_mfma_f32_16x16x32_bf16 v[92:95], v[162:165], v[228:231], v[92:95]
	v_mfma_f32_16x16x32_bf16 v[80:83], v[154:157], v[242:245], v[80:83]
	v_mfma_f32_16x16x32_bf16 v[76:79], v[162:165], v[242:245], v[76:79]
	v_mfma_f32_16x16x32_bf16 v[120:123], v[166:169], v[182:185], v[120:123]
	v_mfma_f32_16x16x32_bf16 v[116:119], v[174:177], v[182:185], v[116:119]
	v_mfma_f32_16x16x32_bf16 v[104:107], v[166:169], v[190:193], v[104:107]
	v_mfma_f32_16x16x32_bf16 v[100:103], v[174:177], v[190:193], v[100:103]
	v_mfma_f32_16x16x32_bf16 v[88:91], v[166:169], v[224:227], v[88:91]
	v_mfma_f32_16x16x32_bf16 v[84:87], v[174:177], v[224:227], v[84:87]
	v_mfma_f32_16x16x32_bf16 v[72:75], v[166:169], v[238:241], v[72:75]
	v_mfma_f32_16x16x32_bf16 v[68:71], v[174:177], v[238:241], v[68:71]
	v_mfma_f32_16x16x32_bf16 v[120:123], v[170:173], v[186:189], v[120:123]
	v_mfma_f32_16x16x32_bf16 v[116:119], v[178:181], v[186:189], v[116:119]
	v_mfma_f32_16x16x32_bf16 v[104:107], v[170:173], v[194:197], v[104:107]
	v_mfma_f32_16x16x32_bf16 v[100:103], v[178:181], v[194:197], v[100:103]
	v_mfma_f32_16x16x32_bf16 v[88:91], v[170:173], v[228:231], v[88:91]
	v_mfma_f32_16x16x32_bf16 v[84:87], v[178:181], v[228:231], v[84:87]
	v_mfma_f32_16x16x32_bf16 v[72:75], v[170:173], v[242:245], v[72:75]
	v_mfma_f32_16x16x32_bf16 v[68:71], v[178:181], v[242:245], v[68:71]
	s_barrier
	s_add_i32 s53, s53, s39
	v_lshl_add_u64 v[198:199], s[34:35], 0, v[34:35]
	s_mov_b32 m0, s53
	s_nop 0
	global_load_lds_dwordx4 v[198:199], off
	s_add_i32 m0, s53, 0x2000
	s_add_u32 s54, s34, 0x80000
	v_lshl_add_u64 v[212:213], s[34:35], 0, v[132:133]
	s_addc_u32 s55, s35, 0
	s_add_i32 s53, s56, s39
	global_load_lds_dwordx4 v[212:213], off
	v_lshl_add_u64 v[232:233], s[54:55], 0, v[34:35]
	s_mov_b32 m0, s53
	v_lshl_add_u64 v[246:247], s[4:5], 0, v[134:135]
	global_load_lds_dwordx4 v[232:233], off
	v_lshl_add_u64 v[232:233], s[54:55], 0, v[132:133]
	s_add_i32 m0, s53, 0x2000
	s_nop 0
	global_load_lds_dwordx4 v[232:233], off
	v_lshl_add_u64 v[232:233], s[4:5], 0, v[138:139]
	s_mov_b32 m0, s42
	s_nop 0
	global_load_lds_dwordx4 v[232:233], off
	s_mov_b32 m0, s43
	s_nop 0
	global_load_lds_dwordx4 v[246:247], off
	ds_read_b128 v[182:185], v152 offset:16384
	ds_read_b128 v[186:189], v152 offset:17408
	ds_read_b128 v[190:193], v152 offset:18432
	ds_read_b128 v[194:197], v152 offset:19456
	ds_read_b128 v[224:227], v152 offset:20480
	ds_read_b128 v[228:231], v152 offset:21504
	ds_read_b128 v[238:241], v152 offset:22528
	ds_read_b128 v[242:245], v152 offset:23552
	s_waitcnt vmcnt(8)
	s_waitcnt lgkmcnt(0)
	s_barrier
	s_waitcnt lgkmcnt(0)
	v_mfma_f32_16x16x32_bf16 v[64:67], v[146:149], v[182:185], v[64:67]
	v_mfma_f32_16x16x32_bf16 v[60:63], v[158:161], v[182:185], v[60:63]
	v_mfma_f32_16x16x32_bf16 v[48:51], v[146:149], v[190:193], v[48:51]
	v_mfma_f32_16x16x32_bf16 v[44:47], v[158:161], v[190:193], v[44:47]
	v_mfma_f32_16x16x32_bf16 v[30:33], v[146:149], v[224:227], v[30:33]
	v_mfma_f32_16x16x32_bf16 v[26:29], v[158:161], v[224:227], v[26:29]
	v_mfma_f32_16x16x32_bf16 v[14:17], v[146:149], v[238:241], v[14:17]
	v_mfma_f32_16x16x32_bf16 v[10:13], v[158:161], v[238:241], v[10:13]
	v_mfma_f32_16x16x32_bf16 v[64:67], v[154:157], v[186:189], v[64:67]
	v_mfma_f32_16x16x32_bf16 v[60:63], v[162:165], v[186:189], v[60:63]
	v_mfma_f32_16x16x32_bf16 v[48:51], v[154:157], v[194:197], v[48:51]
	v_mfma_f32_16x16x32_bf16 v[44:47], v[162:165], v[194:197], v[44:47]
	v_mfma_f32_16x16x32_bf16 v[30:33], v[154:157], v[228:231], v[30:33]
	v_mfma_f32_16x16x32_bf16 v[26:29], v[162:165], v[228:231], v[26:29]
	v_mfma_f32_16x16x32_bf16 v[14:17], v[154:157], v[242:245], v[14:17]
	v_mfma_f32_16x16x32_bf16 v[10:13], v[162:165], v[242:245], v[10:13]
	v_mfma_f32_16x16x32_bf16 v[56:59], v[166:169], v[182:185], v[56:59]
	v_mfma_f32_16x16x32_bf16 v[52:55], v[174:177], v[182:185], v[52:55]
	v_mfma_f32_16x16x32_bf16 v[40:43], v[166:169], v[190:193], v[40:43]
	v_mfma_f32_16x16x32_bf16 v[36:39], v[174:177], v[190:193], v[36:39]
	v_mfma_f32_16x16x32_bf16 v[22:25], v[166:169], v[224:227], v[22:25]
	v_mfma_f32_16x16x32_bf16 v[18:21], v[174:177], v[224:227], v[18:21]
	v_mfma_f32_16x16x32_bf16 v[6:9], v[166:169], v[238:241], v[6:9]
	v_mfma_f32_16x16x32_bf16 v[2:5], v[174:177], v[238:241], v[2:5]
	v_mfma_f32_16x16x32_bf16 v[56:59], v[170:173], v[186:189], v[56:59]
	v_mfma_f32_16x16x32_bf16 v[52:55], v[178:181], v[186:189], v[52:55]
	v_mfma_f32_16x16x32_bf16 v[40:43], v[170:173], v[194:197], v[40:43]
	v_mfma_f32_16x16x32_bf16 v[36:39], v[178:181], v[194:197], v[36:39]
	v_mfma_f32_16x16x32_bf16 v[22:25], v[170:173], v[228:231], v[22:25]
	v_mfma_f32_16x16x32_bf16 v[18:21], v[178:181], v[228:231], v[18:21]
	v_mfma_f32_16x16x32_bf16 v[6:9], v[170:173], v[242:245], v[6:9]
	v_mfma_f32_16x16x32_bf16 v[2:5], v[178:181], v[242:245], v[2:5]
	s_barrier
	s_add_i32 s53, 0, 0x18000
	s_add_i32 s54, 0, 0x1c000
	s_mov_b32 m0, s44
	v_lshl_add_u64 v[248:249], s[4:5], 0, v[140:141]
	global_load_lds_dwordx4 v[248:249], off
	v_lshl_add_u64 v[248:249], s[4:5], 0, v[136:137]
	s_mov_b32 m0, s45
	s_nop 0
	global_load_lds_dwordx4 v[248:249], off
	v_add_u32_e32 v153, s53, v150
	ds_read_b128 v[146:149], v153
	ds_read_b128 v[154:157], v153 offset:1024
	ds_read_b128 v[158:161], v153 offset:2048
	ds_read_b128 v[162:165], v153 offset:3072
	v_add_u32_e32 v153, s54, v150
	ds_read_b128 v[166:169], v153
	ds_read_b128 v[170:173], v153 offset:1024
	ds_read_b128 v[174:177], v153 offset:2048
	ds_read_b128 v[178:181], v153 offset:3072
	ds_read_b128 v[182:185], v152 offset:32768
	ds_read_b128 v[186:189], v152 offset:33792
	ds_read_b128 v[190:193], v152 offset:34816
	ds_read_b128 v[194:197], v152 offset:35840
	ds_read_b128 v[224:227], v152 offset:36864
	ds_read_b128 v[228:231], v152 offset:37888
	ds_read_b128 v[238:241], v152 offset:38912
	ds_read_b128 v[242:245], v152 offset:39936
	s_waitcnt vmcnt(8)
	s_waitcnt lgkmcnt(0)
	s_barrier
	s_waitcnt lgkmcnt(0)
	v_mfma_f32_16x16x32_bf16 v[128:131], v[146:149], v[182:185], v[128:131]
	v_mfma_f32_16x16x32_bf16 v[124:127], v[158:161], v[182:185], v[124:127]
	v_mfma_f32_16x16x32_bf16 v[112:115], v[146:149], v[190:193], v[112:115]
	v_mfma_f32_16x16x32_bf16 v[108:111], v[158:161], v[190:193], v[108:111]
	v_mfma_f32_16x16x32_bf16 v[96:99], v[146:149], v[224:227], v[96:99]
	v_mfma_f32_16x16x32_bf16 v[92:95], v[158:161], v[224:227], v[92:95]
	v_mfma_f32_16x16x32_bf16 v[80:83], v[146:149], v[238:241], v[80:83]
	v_mfma_f32_16x16x32_bf16 v[76:79], v[158:161], v[238:241], v[76:79]
	v_mfma_f32_16x16x32_bf16 v[128:131], v[154:157], v[186:189], v[128:131]
	v_mfma_f32_16x16x32_bf16 v[124:127], v[162:165], v[186:189], v[124:127]
	v_mfma_f32_16x16x32_bf16 v[112:115], v[154:157], v[194:197], v[112:115]
	v_mfma_f32_16x16x32_bf16 v[108:111], v[162:165], v[194:197], v[108:111]
	v_mfma_f32_16x16x32_bf16 v[96:99], v[154:157], v[228:231], v[96:99]
	v_mfma_f32_16x16x32_bf16 v[92:95], v[162:165], v[228:231], v[92:95]
	v_mfma_f32_16x16x32_bf16 v[80:83], v[154:157], v[242:245], v[80:83]
	v_mfma_f32_16x16x32_bf16 v[76:79], v[162:165], v[242:245], v[76:79]
	v_mfma_f32_16x16x32_bf16 v[120:123], v[166:169], v[182:185], v[120:123]
	v_mfma_f32_16x16x32_bf16 v[116:119], v[174:177], v[182:185], v[116:119]
	v_mfma_f32_16x16x32_bf16 v[104:107], v[166:169], v[190:193], v[104:107]
	v_mfma_f32_16x16x32_bf16 v[100:103], v[174:177], v[190:193], v[100:103]
	v_mfma_f32_16x16x32_bf16 v[88:91], v[166:169], v[224:227], v[88:91]
	v_mfma_f32_16x16x32_bf16 v[84:87], v[174:177], v[224:227], v[84:87]
	v_mfma_f32_16x16x32_bf16 v[72:75], v[166:169], v[238:241], v[72:75]
	v_mfma_f32_16x16x32_bf16 v[68:71], v[174:177], v[238:241], v[68:71]
	v_mfma_f32_16x16x32_bf16 v[120:123], v[170:173], v[186:189], v[120:123]
	v_mfma_f32_16x16x32_bf16 v[116:119], v[178:181], v[186:189], v[116:119]
	v_mfma_f32_16x16x32_bf16 v[104:107], v[170:173], v[194:197], v[104:107]
	v_mfma_f32_16x16x32_bf16 v[100:103], v[178:181], v[194:197], v[100:103]
	v_mfma_f32_16x16x32_bf16 v[88:91], v[170:173], v[228:231], v[88:91]
	v_mfma_f32_16x16x32_bf16 v[84:87], v[178:181], v[228:231], v[84:87]
	v_mfma_f32_16x16x32_bf16 v[72:75], v[170:173], v[242:245], v[72:75]
	v_mfma_f32_16x16x32_bf16 v[68:71], v[178:181], v[242:245], v[68:71]
	s_barrier
	s_add_i32 s4, s53, s39
	v_lshl_add_u64 v[198:199], v[198:199], 0, s[78:79]
	s_mov_b32 m0, s4
	s_nop 0
	global_load_lds_dwordx4 v[198:199], off
	s_add_i32 m0, s4, 0x2000
	s_add_u32 s4, s34, 0x80080
	v_lshl_add_u64 v[198:199], v[212:213], 0, s[78:79]
	s_addc_u32 s5, s35, 0
	s_add_i32 s34, s54, s39
	global_load_lds_dwordx4 v[198:199], off
	v_lshl_add_u64 v[198:199], s[4:5], 0, v[34:35]
	s_mov_b32 m0, s34
	s_nop 0
	global_load_lds_dwordx4 v[198:199], off
	v_lshl_add_u64 v[198:199], s[4:5], 0, v[132:133]
	s_add_i32 m0, s34, 0x2000
	s_nop 0
	global_load_lds_dwordx4 v[198:199], off
	v_lshl_add_u64 v[198:199], v[232:233], 0, s[78:79]
	s_mov_b32 m0, s46
	s_nop 0
	global_load_lds_dwordx4 v[198:199], off
	v_lshl_add_u64 v[198:199], v[246:247], 0, s[78:79]
	s_mov_b32 m0, s47
	s_nop 0
	global_load_lds_dwordx4 v[198:199], off
	ds_read_b128 v[182:185], v152 offset:49152
	ds_read_b128 v[186:189], v152 offset:50176
	ds_read_b128 v[190:193], v152 offset:51200
	ds_read_b128 v[194:197], v152 offset:52224
	ds_read_b128 v[224:227], v152 offset:53248
	ds_read_b128 v[228:231], v152 offset:54272
	ds_read_b128 v[238:241], v152 offset:55296
	ds_read_b128 v[242:245], v152 offset:56320
	s_waitcnt vmcnt(8)
	s_waitcnt lgkmcnt(0)
	s_barrier
	s_waitcnt lgkmcnt(0)
	v_mfma_f32_16x16x32_bf16 v[64:67], v[146:149], v[182:185], v[64:67]
	v_mfma_f32_16x16x32_bf16 v[60:63], v[158:161], v[182:185], v[60:63]
	v_mfma_f32_16x16x32_bf16 v[48:51], v[146:149], v[190:193], v[48:51]
	v_mfma_f32_16x16x32_bf16 v[44:47], v[158:161], v[190:193], v[44:47]
	v_mfma_f32_16x16x32_bf16 v[30:33], v[146:149], v[224:227], v[30:33]
	v_mfma_f32_16x16x32_bf16 v[26:29], v[158:161], v[224:227], v[26:29]
	v_mfma_f32_16x16x32_bf16 v[14:17], v[146:149], v[238:241], v[14:17]
	v_mfma_f32_16x16x32_bf16 v[10:13], v[158:161], v[238:241], v[10:13]
	v_mfma_f32_16x16x32_bf16 v[64:67], v[154:157], v[186:189], v[64:67]
	v_mfma_f32_16x16x32_bf16 v[60:63], v[162:165], v[186:189], v[60:63]
	v_mfma_f32_16x16x32_bf16 v[48:51], v[154:157], v[194:197], v[48:51]
	v_mfma_f32_16x16x32_bf16 v[44:47], v[162:165], v[194:197], v[44:47]
	v_mfma_f32_16x16x32_bf16 v[30:33], v[154:157], v[228:231], v[30:33]
	v_mfma_f32_16x16x32_bf16 v[26:29], v[162:165], v[228:231], v[26:29]
	v_mfma_f32_16x16x32_bf16 v[14:17], v[154:157], v[242:245], v[14:17]
	v_mfma_f32_16x16x32_bf16 v[10:13], v[162:165], v[242:245], v[10:13]
	v_mfma_f32_16x16x32_bf16 v[56:59], v[166:169], v[182:185], v[56:59]
	v_mfma_f32_16x16x32_bf16 v[52:55], v[174:177], v[182:185], v[52:55]
	v_mfma_f32_16x16x32_bf16 v[40:43], v[166:169], v[190:193], v[40:43]
	v_mfma_f32_16x16x32_bf16 v[36:39], v[174:177], v[190:193], v[36:39]
	v_mfma_f32_16x16x32_bf16 v[22:25], v[166:169], v[224:227], v[22:25]
	v_mfma_f32_16x16x32_bf16 v[18:21], v[174:177], v[224:227], v[18:21]
	v_mfma_f32_16x16x32_bf16 v[6:9], v[166:169], v[238:241], v[6:9]
	v_mfma_f32_16x16x32_bf16 v[2:5], v[174:177], v[238:241], v[2:5]
	v_mfma_f32_16x16x32_bf16 v[56:59], v[170:173], v[186:189], v[56:59]
	v_mfma_f32_16x16x32_bf16 v[52:55], v[178:181], v[186:189], v[52:55]
	v_mfma_f32_16x16x32_bf16 v[40:43], v[170:173], v[194:197], v[40:43]
	v_mfma_f32_16x16x32_bf16 v[36:39], v[178:181], v[194:197], v[36:39]
	v_mfma_f32_16x16x32_bf16 v[22:25], v[170:173], v[228:231], v[22:25]
	v_mfma_f32_16x16x32_bf16 v[18:21], v[178:181], v[228:231], v[18:21]
	v_mfma_f32_16x16x32_bf16 v[6:9], v[170:173], v[242:245], v[6:9]
	v_mfma_f32_16x16x32_bf16 v[2:5], v[178:181], v[242:245], v[2:5]
	s_barrier
	s_add_i32 s52, s52, 2
	s_add_u32 s23, s23, 0x100
	s_addc_u32 s25, s25, 0
	s_add_u32 s30, s30, 0x100
	s_addc_u32 s31, s31, 0
	s_cmp_gt_u32 s52, 29
	s_cbranch_scc0 .LBB0_607
	s_setprio 0
	s_and_b64 vcc, exec, s[20:21]
	s_cbranch_vccz .LBB0_610
	s_barrier

.Lsp673:
.LBB0_673:
	s_add_u32 s4, s30, 0x80
	s_addc_u32 s5, s31, 0
	s_add_i32 s64, 0, 0x10000
	s_cmp_eq_u32 s57, 12
	s_cselect_b32 s5, s27, s5
	s_cselect_b32 s4, s26, s4
	s_cselect_b32 s35, s29, s25
	s_cselect_b32 s34, s28, s23
	s_add_i32 s68, 0, 0x14000
	v_lshl_add_u64 v[164:165], s[30:31], 0, v[178:179]
	s_add_i32 m0, s38, 0xc000
	s_nop 0
	global_load_lds_dwordx4 v[164:165], off
	v_lshl_add_u64 v[164:165], s[30:31], 0, v[176:177]
	s_add_i32 m0, s38, 0xe000
	s_nop 0
	global_load_lds_dwordx4 v[164:165], off
	v_add_u32_e32 v144, s64, v190
	v_add_u32_e32 v160, s68, v190
	ds_read_b128 v[132:135], v144
	ds_read_b128 v[136:139], v144 offset:1024
	ds_read_b128 v[140:143], v144 offset:2048
	ds_read_b128 v[144:147], v144 offset:3072
	ds_read_b128 v[148:151], v160
	ds_read_b128 v[152:155], v160 offset:1024
	ds_read_b128 v[156:159], v160 offset:2048
	ds_read_b128 v[160:163], v160 offset:3072
	ds_read_b128 v[180:183], v192
	ds_read_b128 v[184:187], v192 offset:1024
	ds_read_b128 v[194:197], v192 offset:2048
	ds_read_b128 v[224:227], v192 offset:3072
	ds_read_b128 v[228:231], v192 offset:4096
	ds_read_b128 v[238:241], v192 offset:5120
	ds_read_b128 v[242:245], v192 offset:6144
	ds_read_b128 v[246:249], v192 offset:7168
	s_waitcnt vmcnt(8)
	s_waitcnt lgkmcnt(0)
	s_barrier
	s_waitcnt lgkmcnt(0)
	v_mfma_f32_16x16x32_bf16 v[128:131], v[132:135], v[180:183], v[128:131]
	v_mfma_f32_16x16x32_bf16 v[124:127], v[140:143], v[180:183], v[124:127]
	v_mfma_f32_16x16x32_bf16 v[112:115], v[132:135], v[194:197], v[112:115]
	v_mfma_f32_16x16x32_bf16 v[108:111], v[140:143], v[194:197], v[108:111]
	v_mfma_f32_16x16x32_bf16 v[96:99], v[132:135], v[228:231], v[96:99]
	v_mfma_f32_16x16x32_bf16 v[92:95], v[140:143], v[228:231], v[92:95]
	v_mfma_f32_16x16x32_bf16 v[80:83], v[132:135], v[242:245], v[80:83]
	v_mfma_f32_16x16x32_bf16 v[76:79], v[140:143], v[242:245], v[76:79]
	v_mfma_f32_16x16x32_bf16 v[128:131], v[136:139], v[184:187], v[128:131]
	v_mfma_f32_16x16x32_bf16 v[124:127], v[144:147], v[184:187], v[124:127]
	v_mfma_f32_16x16x32_bf16 v[112:115], v[136:139], v[224:227], v[112:115]
	v_mfma_f32_16x16x32_bf16 v[108:111], v[144:147], v[224:227], v[108:111]
	v_mfma_f32_16x16x32_bf16 v[96:99], v[136:139], v[238:241], v[96:99]
	v_mfma_f32_16x16x32_bf16 v[92:95], v[144:147], v[238:241], v[92:95]
	v_mfma_f32_16x16x32_bf16 v[80:83], v[136:139], v[246:249], v[80:83]
	v_mfma_f32_16x16x32_bf16 v[76:79], v[144:147], v[246:249], v[76:79]
	v_mfma_f32_16x16x32_bf16 v[120:123], v[148:151], v[180:183], v[120:123]
	v_mfma_f32_16x16x32_bf16 v[116:119], v[156:159], v[180:183], v[116:119]
	v_mfma_f32_16x16x32_bf16 v[104:107], v[148:151], v[194:197], v[104:107]
	v_mfma_f32_16x16x32_bf16 v[100:103], v[156:159], v[194:197], v[100:103]
	v_mfma_f32_16x16x32_bf16 v[88:91], v[148:151], v[228:231], v[88:91]
	v_mfma_f32_16x16x32_bf16 v[84:87], v[156:159], v[228:231], v[84:87]
	v_mfma_f32_16x16x32_bf16 v[72:75], v[148:151], v[242:245], v[72:75]
	v_mfma_f32_16x16x32_bf16 v[68:71], v[156:159], v[242:245], v[68:71]
	v_mfma_f32_16x16x32_bf16 v[120:123], v[152:155], v[184:187], v[120:123]
	v_mfma_f32_16x16x32_bf16 v[116:119], v[160:163], v[184:187], v[116:119]
	v_mfma_f32_16x16x32_bf16 v[104:107], v[152:155], v[224:227], v[104:107]
	v_mfma_f32_16x16x32_bf16 v[100:103], v[160:163], v[224:227], v[100:103]
	v_mfma_f32_16x16x32_bf16 v[88:91], v[152:155], v[238:241], v[88:91]
	v_mfma_f32_16x16x32_bf16 v[84:87], v[160:163], v[238:241], v[84:87]
	v_mfma_f32_16x16x32_bf16 v[72:75], v[152:155], v[246:249], v[72:75]
	v_mfma_f32_16x16x32_bf16 v[68:71], v[160:163], v[246:249], v[68:71]
	s_barrier
	s_add_i32 s64, s64, s37
	v_lshl_add_u64 v[164:165], s[34:35], 0, v[34:35]
	s_mov_b32 m0, s64
	s_nop 0
	global_load_lds_dwordx4 v[164:165], off
	s_add_i32 m0, s64, 0x2000
	s_add_u32 s64, s34, 0x40000
	v_lshl_add_u64 v[188:189], s[34:35], 0, v[174:175]
	s_addc_u32 s65, s35, 0
	s_add_i32 s68, s68, s37
	global_load_lds_dwordx4 v[188:189], off
	v_lshl_add_u64 v[198:199], s[64:65], 0, v[34:35]
	s_mov_b32 m0, s68
	v_lshl_add_u64 v[212:213], s[4:5], 0, v[170:171]
	global_load_lds_dwordx4 v[198:199], off
	v_lshl_add_u64 v[198:199], s[64:65], 0, v[174:175]
	s_add_i32 m0, s68, 0x2000
	s_nop 0
	global_load_lds_dwordx4 v[198:199], off
	v_lshl_add_u64 v[198:199], s[4:5], 0, v[166:167]
	s_mov_b32 m0, s38
	s_nop 0
	global_load_lds_dwordx4 v[198:199], off
	s_mov_b32 m0, s39
	s_nop 0
	global_load_lds_dwordx4 v[212:213], off
	ds_read_b128 v[180:183], v192 offset:16384
	ds_read_b128 v[184:187], v192 offset:17408
	ds_read_b128 v[194:197], v192 offset:18432
	ds_read_b128 v[224:227], v192 offset:19456
	ds_read_b128 v[228:231], v192 offset:20480
	ds_read_b128 v[238:241], v192 offset:21504
	ds_read_b128 v[242:245], v192 offset:22528
	ds_read_b128 v[246:249], v192 offset:23552
	s_waitcnt vmcnt(8)
	s_waitcnt lgkmcnt(0)
	s_barrier
	s_waitcnt lgkmcnt(0)
	v_mfma_f32_16x16x32_bf16 v[64:67], v[132:135], v[180:183], v[64:67]
	v_mfma_f32_16x16x32_bf16 v[60:63], v[140:143], v[180:183], v[60:63]
	v_mfma_f32_16x16x32_bf16 v[48:51], v[132:135], v[194:197], v[48:51]
	v_mfma_f32_16x16x32_bf16 v[44:47], v[140:143], v[194:197], v[44:47]
	v_mfma_f32_16x16x32_bf16 v[30:33], v[132:135], v[228:231], v[30:33]
	v_mfma_f32_16x16x32_bf16 v[26:29], v[140:143], v[228:231], v[26:29]
	v_mfma_f32_16x16x32_bf16 v[14:17], v[132:135], v[242:245], v[14:17]
	v_mfma_f32_16x16x32_bf16 v[10:13], v[140:143], v[242:245], v[10:13]
	v_mfma_f32_16x16x32_bf16 v[64:67], v[136:139], v[184:187], v[64:67]
	v_mfma_f32_16x16x32_bf16 v[60:63], v[144:147], v[184:187], v[60:63]
	v_mfma_f32_16x16x32_bf16 v[48:51], v[136:139], v[224:227], v[48:51]
	v_mfma_f32_16x16x32_bf16 v[44:47], v[144:147], v[224:227], v[44:47]
	v_mfma_f32_16x16x32_bf16 v[30:33], v[136:139], v[238:241], v[30:33]
	v_mfma_f32_16x16x32_bf16 v[26:29], v[144:147], v[238:241], v[26:29]
	v_mfma_f32_16x16x32_bf16 v[14:17], v[136:139], v[246:249], v[14:17]
	v_mfma_f32_16x16x32_bf16 v[10:13], v[144:147], v[246:249], v[10:13]
	v_mfma_f32_16x16x32_bf16 v[56:59], v[148:151], v[180:183], v[56:59]
	v_mfma_f32_16x16x32_bf16 v[52:55], v[156:159], v[180:183], v[52:55]
	v_mfma_f32_16x16x32_bf16 v[40:43], v[148:151], v[194:197], v[40:43]
	v_mfma_f32_16x16x32_bf16 v[36:39], v[156:159], v[194:197], v[36:39]
	v_mfma_f32_16x16x32_bf16 v[22:25], v[148:151], v[228:231], v[22:25]
	v_mfma_f32_16x16x32_bf16 v[18:21], v[156:159], v[228:231], v[18:21]
	v_mfma_f32_16x16x32_bf16 v[6:9], v[148:151], v[242:245], v[6:9]
	v_mfma_f32_16x16x32_bf16 v[2:5], v[156:159], v[242:245], v[2:5]
	v_mfma_f32_16x16x32_bf16 v[56:59], v[152:155], v[184:187], v[56:59]
	v_mfma_f32_16x16x32_bf16 v[52:55], v[160:163], v[184:187], v[52:55]
	v_mfma_f32_16x16x32_bf16 v[40:43], v[152:155], v[224:227], v[40:43]
	v_mfma_f32_16x16x32_bf16 v[36:39], v[160:163], v[224:227], v[36:39]
	v_mfma_f32_16x16x32_bf16 v[22:25], v[152:155], v[238:241], v[22:25]
	v_mfma_f32_16x16x32_bf16 v[18:21], v[160:163], v[238:241], v[18:21]
	v_mfma_f32_16x16x32_bf16 v[6:9], v[152:155], v[246:249], v[6:9]
	v_mfma_f32_16x16x32_bf16 v[2:5], v[160:163], v[246:249], v[2:5]
	s_barrier
	s_add_i32 s64, 0, 0x18000
	s_add_i32 s65, 0, 0x1c000
	s_mov_b32 m0, s46
	v_lshl_add_u64 v[232:233], s[4:5], 0, v[168:169]
	global_load_lds_dwordx4 v[232:233], off
	v_lshl_add_u64 v[232:233], s[4:5], 0, v[172:173]
	s_mov_b32 m0, s47
	s_nop 0
	global_load_lds_dwordx4 v[232:233], off
	v_add_u32_e32 v144, s64, v190
	v_add_u32_e32 v160, s65, v190
	ds_read_b128 v[132:135], v144
	ds_read_b128 v[136:139], v144 offset:1024
	ds_read_b128 v[140:143], v144 offset:2048
	ds_read_b128 v[144:147], v144 offset:3072
	ds_read_b128 v[148:151], v160
	ds_read_b128 v[152:155], v160 offset:1024
	ds_read_b128 v[156:159], v160 offset:2048
	ds_read_b128 v[160:163], v160 offset:3072
	ds_read_b128 v[180:183], v192 offset:32768
	ds_read_b128 v[184:187], v192 offset:33792
	ds_read_b128 v[194:197], v192 offset:34816
	ds_read_b128 v[224:227], v192 offset:35840
	ds_read_b128 v[228:231], v192 offset:36864
	ds_read_b128 v[238:241], v192 offset:37888
	ds_read_b128 v[242:245], v192 offset:38912
	ds_read_b128 v[246:249], v192 offset:39936
	s_waitcnt vmcnt(8)
	s_waitcnt lgkmcnt(0)
	s_barrier
	s_waitcnt lgkmcnt(0)
	v_mfma_f32_16x16x32_bf16 v[128:131], v[132:135], v[180:183], v[128:131]
	v_mfma_f32_16x16x32_bf16 v[124:127], v[140:143], v[180:183], v[124:127]
	v_mfma_f32_16x16x32_bf16 v[112:115], v[132:135], v[194:197], v[112:115]
	v_mfma_f32_16x16x32_bf16 v[108:111], v[140:143], v[194:197], v[108:111]
	v_mfma_f32_16x16x32_bf16 v[96:99], v[132:135], v[228:231], v[96:99]
	v_mfma_f32_16x16x32_bf16 v[92:95], v[140:143], v[228:231], v[92:95]
	v_mfma_f32_16x16x32_bf16 v[80:83], v[132:135], v[242:245], v[80:83]
	v_mfma_f32_16x16x32_bf16 v[76:79], v[140:143], v[242:245], v[76:79]
	v_mfma_f32_16x16x32_bf16 v[128:131], v[136:139], v[184:187], v[128:131]
	v_mfma_f32_16x16x32_bf16 v[124:127], v[144:147], v[184:187], v[124:127]
	v_mfma_f32_16x16x32_bf16 v[112:115], v[136:139], v[224:227], v[112:115]
	v_mfma_f32_16x16x32_bf16 v[108:111], v[144:147], v[224:227], v[108:111]
	v_mfma_f32_16x16x32_bf16 v[96:99], v[136:139], v[238:241], v[96:99]
	v_mfma_f32_16x16x32_bf16 v[92:95], v[144:147], v[238:241], v[92:95]
	v_mfma_f32_16x16x32_bf16 v[80:83], v[136:139], v[246:249], v[80:83]
	v_mfma_f32_16x16x32_bf16 v[76:79], v[144:147], v[246:249], v[76:79]
	v_mfma_f32_16x16x32_bf16 v[120:123], v[148:151], v[180:183], v[120:123]
	v_mfma_f32_16x16x32_bf16 v[116:119], v[156:159], v[180:183], v[116:119]
	v_mfma_f32_16x16x32_bf16 v[104:107], v[148:151], v[194:197], v[104:107]
	v_mfma_f32_16x16x32_bf16 v[100:103], v[156:159], v[194:197], v[100:103]
	v_mfma_f32_16x16x32_bf16 v[88:91], v[148:151], v[228:231], v[88:91]
	v_mfma_f32_16x16x32_bf16 v[84:87], v[156:159], v[228:231], v[84:87]
	v_mfma_f32_16x16x32_bf16 v[72:75], v[148:151], v[242:245], v[72:75]
	v_mfma_f32_16x16x32_bf16 v[68:71], v[156:159], v[242:245], v[68:71]
	v_mfma_f32_16x16x32_bf16 v[120:123], v[152:155], v[184:187], v[120:123]
	v_mfma_f32_16x16x32_bf16 v[116:119], v[160:163], v[184:187], v[116:119]
	v_mfma_f32_16x16x32_bf16 v[104:107], v[152:155], v[224:227], v[104:107]
	v_mfma_f32_16x16x32_bf16 v[100:103], v[160:163], v[224:227], v[100:103]
	v_mfma_f32_16x16x32_bf16 v[88:91], v[152:155], v[238:241], v[88:91]
	v_mfma_f32_16x16x32_bf16 v[84:87], v[160:163], v[238:241], v[84:87]
	v_mfma_f32_16x16x32_bf16 v[72:75], v[152:155], v[246:249], v[72:75]
	v_mfma_f32_16x16x32_bf16 v[68:71], v[160:163], v[246:249], v[68:71]
	s_barrier
	s_add_i32 s4, s64, s37
	v_lshl_add_u64 v[164:165], v[164:165], 0, s[78:79]
	s_mov_b32 m0, s4
	s_nop 0
	global_load_lds_dwordx4 v[164:165], off
	s_add_i32 m0, s4, 0x2000
	s_add_u32 s4, s34, 0x40080
	v_lshl_add_u64 v[164:165], v[188:189], 0, s[78:79]
	s_addc_u32 s5, s35, 0
	s_add_i32 s34, s65, s37
	global_load_lds_dwordx4 v[164:165], off
	v_lshl_add_u64 v[164:165], s[4:5], 0, v[34:35]
	s_mov_b32 m0, s34
	s_nop 0
	global_load_lds_dwordx4 v[164:165], off
	v_lshl_add_u64 v[164:165], s[4:5], 0, v[174:175]
	s_add_i32 m0, s34, 0x2000
	s_nop 0
	global_load_lds_dwordx4 v[164:165], off
	v_lshl_add_u64 v[164:165], v[198:199], 0, s[78:79]
	s_mov_b32 m0, s52
	s_nop 0
	global_load_lds_dwordx4 v[164:165], off
	v_lshl_add_u64 v[164:165], v[212:213], 0, s[78:79]
	s_mov_b32 m0, s53
	s_nop 0
	global_load_lds_dwordx4 v[164:165], off
	ds_read_b128 v[180:183], v192 offset:49152
	ds_read_b128 v[184:187], v192 offset:50176
	ds_read_b128 v[194:197], v192 offset:51200
	ds_read_b128 v[224:227], v192 offset:52224
	ds_read_b128 v[228:231], v192 offset:53248
	ds_read_b128 v[238:241], v192 offset:54272
	ds_read_b128 v[242:245], v192 offset:55296
	ds_read_b128 v[246:249], v192 offset:56320
	s_waitcnt vmcnt(8)
	s_waitcnt lgkmcnt(0)
	s_barrier
	s_waitcnt lgkmcnt(0)
	v_mfma_f32_16x16x32_bf16 v[64:67], v[132:135], v[180:183], v[64:67]
	v_mfma_f32_16x16x32_bf16 v[60:63], v[140:143], v[180:183], v[60:63]
	v_mfma_f32_16x16x32_bf16 v[48:51], v[132:135], v[194:197], v[48:51]
	v_mfma_f32_16x16x32_bf16 v[44:47], v[140:143], v[194:197], v[44:47]
	v_mfma_f32_16x16x32_bf16 v[30:33], v[132:135], v[228:231], v[30:33]
	v_mfma_f32_16x16x32_bf16 v[26:29], v[140:143], v[228:231], v[26:29]
	v_mfma_f32_16x16x32_bf16 v[14:17], v[132:135], v[242:245], v[14:17]
	v_mfma_f32_16x16x32_bf16 v[10:13], v[140:143], v[242:245], v[10:13]
	v_mfma_f32_16x16x32_bf16 v[64:67], v[136:139], v[184:187], v[64:67]
	v_mfma_f32_16x16x32_bf16 v[60:63], v[144:147], v[184:187], v[60:63]
	v_mfma_f32_16x16x32_bf16 v[48:51], v[136:139], v[224:227], v[48:51]
	v_mfma_f32_16x16x32_bf16 v[44:47], v[144:147], v[224:227], v[44:47]
	v_mfma_f32_16x16x32_bf16 v[30:33], v[136:139], v[238:241], v[30:33]
	v_mfma_f32_16x16x32_bf16 v[26:29], v[144:147], v[238:241], v[26:29]
	v_mfma_f32_16x16x32_bf16 v[14:17], v[136:139], v[246:249], v[14:17]
	v_mfma_f32_16x16x32_bf16 v[10:13], v[144:147], v[246:249], v[10:13]
	v_mfma_f32_16x16x32_bf16 v[56:59], v[148:151], v[180:183], v[56:59]
	v_mfma_f32_16x16x32_bf16 v[52:55], v[156:159], v[180:183], v[52:55]
	v_mfma_f32_16x16x32_bf16 v[40:43], v[148:151], v[194:197], v[40:43]
	v_mfma_f32_16x16x32_bf16 v[36:39], v[156:159], v[194:197], v[36:39]
	v_mfma_f32_16x16x32_bf16 v[22:25], v[148:151], v[228:231], v[22:25]
	v_mfma_f32_16x16x32_bf16 v[18:21], v[156:159], v[228:231], v[18:21]
	v_mfma_f32_16x16x32_bf16 v[6:9], v[148:151], v[242:245], v[6:9]
	v_mfma_f32_16x16x32_bf16 v[2:5], v[156:159], v[242:245], v[2:5]
	v_mfma_f32_16x16x32_bf16 v[56:59], v[152:155], v[184:187], v[56:59]
	v_mfma_f32_16x16x32_bf16 v[52:55], v[160:163], v[184:187], v[52:55]
	v_mfma_f32_16x16x32_bf16 v[40:43], v[152:155], v[224:227], v[40:43]
	v_mfma_f32_16x16x32_bf16 v[36:39], v[160:163], v[224:227], v[36:39]
	v_mfma_f32_16x16x32_bf16 v[22:25], v[152:155], v[238:241], v[22:25]
	v_mfma_f32_16x16x32_bf16 v[18:21], v[160:163], v[238:241], v[18:21]
	v_mfma_f32_16x16x32_bf16 v[6:9], v[152:155], v[246:249], v[6:9]
	v_mfma_f32_16x16x32_bf16 v[2:5], v[160:163], v[246:249], v[2:5]
	s_barrier
	s_add_i32 s57, s57, 2
	s_add_u32 s23, s23, 0x100
	s_addc_u32 s25, s25, 0
	s_add_u32 s30, s30, 0x100
	s_addc_u32 s31, s31, 0
	s_cmp_gt_u32 s57, 13
	s_cbranch_scc0 .LBB0_673
	s_setprio 0
	s_and_b64 vcc, exec, s[20:21]
	s_cbranch_vccz .LBB0_676
	s_barrier

.Lsp787:
.LBB0_787:
	s_add_u32 s4, s38, 0x80
	s_addc_u32 s5, s39, 0
	s_add_i32 s69, 0, 0x10000
	s_cmp_eq_u32 s68, 28
	s_cselect_b32 s5, s35, s5
	s_cselect_b32 s4, s34, s4
	s_cselect_b32 s45, s37, s31
	s_cselect_b32 s44, s36, s29
	s_add_i32 s74, 0, 0x14000
	v_lshl_add_u64 v[198:199], s[38:39], 0, v[152:153]
	s_add_i32 m0, s50, 0xc000
	s_nop 0
	global_load_lds_dwordx4 v[198:199], off
	v_lshl_add_u64 v[198:199], s[38:39], 0, v[150:151]
	s_add_i32 m0, s50, 0xe000
	s_nop 0
	global_load_lds_dwordx4 v[198:199], off
	v_add_u32_e32 v154, s69, v162
	v_add_u32_e32 v165, s74, v162
	ds_read_b128 v[132:135], v154
	ds_read_b128 v[136:139], v154 offset:1024
	ds_read_b128 v[140:143], v154 offset:2048
	ds_read_b128 v[154:157], v154 offset:3072
	ds_read_b128 v[158:161], v165
	ds_read_b128 v[166:169], v165 offset:1024
	ds_read_b128 v[170:173], v165 offset:2048
	ds_read_b128 v[174:177], v165 offset:3072
	ds_read_b128 v[178:181], v164
	ds_read_b128 v[182:185], v164 offset:1024
	ds_read_b128 v[186:189], v164 offset:2048
	ds_read_b128 v[190:193], v164 offset:3072
	ds_read_b128 v[194:197], v164 offset:4096
	ds_read_b128 v[224:227], v164 offset:5120
	ds_read_b128 v[228:231], v164 offset:6144
	ds_read_b128 v[238:241], v164 offset:7168
	s_waitcnt vmcnt(8)
	s_waitcnt lgkmcnt(0)
	s_barrier
	s_waitcnt lgkmcnt(0)
	v_mfma_f32_16x16x32_bf16 v[128:131], v[132:135], v[178:181], v[128:131]
	v_mfma_f32_16x16x32_bf16 v[124:127], v[140:143], v[178:181], v[124:127]
	v_mfma_f32_16x16x32_bf16 v[120:123], v[132:135], v[186:189], v[120:123]
	v_mfma_f32_16x16x32_bf16 v[108:111], v[140:143], v[186:189], v[108:111]
	v_mfma_f32_16x16x32_bf16 v[104:107], v[132:135], v[194:197], v[104:107]
	v_mfma_f32_16x16x32_bf16 v[92:95], v[140:143], v[194:197], v[92:95]
	v_mfma_f32_16x16x32_bf16 v[88:91], v[132:135], v[228:231], v[88:91]
	v_mfma_f32_16x16x32_bf16 v[76:79], v[140:143], v[228:231], v[76:79]
	v_mfma_f32_16x16x32_bf16 v[128:131], v[136:139], v[182:185], v[128:131]
	v_mfma_f32_16x16x32_bf16 v[124:127], v[154:157], v[182:185], v[124:127]
	v_mfma_f32_16x16x32_bf16 v[120:123], v[136:139], v[190:193], v[120:123]
	v_mfma_f32_16x16x32_bf16 v[108:111], v[154:157], v[190:193], v[108:111]
	v_mfma_f32_16x16x32_bf16 v[104:107], v[136:139], v[224:227], v[104:107]
	v_mfma_f32_16x16x32_bf16 v[92:95], v[154:157], v[224:227], v[92:95]
	v_mfma_f32_16x16x32_bf16 v[88:91], v[136:139], v[238:241], v[88:91]
	v_mfma_f32_16x16x32_bf16 v[76:79], v[154:157], v[238:241], v[76:79]
	v_mfma_f32_16x16x32_bf16 v[116:119], v[158:161], v[178:181], v[116:119]
	v_mfma_f32_16x16x32_bf16 v[112:115], v[170:173], v[178:181], v[112:115]
	v_mfma_f32_16x16x32_bf16 v[100:103], v[158:161], v[186:189], v[100:103]
	v_mfma_f32_16x16x32_bf16 v[96:99], v[170:173], v[186:189], v[96:99]
	v_mfma_f32_16x16x32_bf16 v[84:87], v[158:161], v[194:197], v[84:87]
	v_mfma_f32_16x16x32_bf16 v[80:83], v[170:173], v[194:197], v[80:83]
	v_mfma_f32_16x16x32_bf16 v[72:75], v[158:161], v[228:231], v[72:75]
	v_mfma_f32_16x16x32_bf16 v[68:71], v[170:173], v[228:231], v[68:71]
	v_mfma_f32_16x16x32_bf16 v[116:119], v[166:169], v[182:185], v[116:119]
	v_mfma_f32_16x16x32_bf16 v[112:115], v[174:177], v[182:185], v[112:115]
	v_mfma_f32_16x16x32_bf16 v[100:103], v[166:169], v[190:193], v[100:103]
	v_mfma_f32_16x16x32_bf16 v[96:99], v[174:177], v[190:193], v[96:99]
	v_mfma_f32_16x16x32_bf16 v[84:87], v[166:169], v[224:227], v[84:87]
	v_mfma_f32_16x16x32_bf16 v[80:83], v[174:177], v[224:227], v[80:83]
	v_mfma_f32_16x16x32_bf16 v[72:75], v[166:169], v[238:241], v[72:75]
	v_mfma_f32_16x16x32_bf16 v[68:71], v[174:177], v[238:241], v[68:71]
	s_barrier
	s_add_i32 s69, s69, s49
	v_lshl_add_u64 v[198:199], s[44:45], 0, v[34:35]
	s_mov_b32 m0, s69
	s_nop 0
	global_load_lds_dwordx4 v[198:199], off
	s_add_i32 m0, s69, 0x2000
	s_add_u32 s70, s44, 0x80000
	v_lshl_add_u64 v[212:213], s[44:45], 0, v[144:145]
	s_addc_u32 s71, s45, 0
	s_add_i32 s69, s74, s49
	global_load_lds_dwordx4 v[212:213], off
	v_lshl_add_u64 v[232:233], s[70:71], 0, v[34:35]
	s_mov_b32 m0, s69
	v_lshl_add_u64 v[242:243], s[4:5], 0, v[144:145]
	global_load_lds_dwordx4 v[232:233], off
	v_lshl_add_u64 v[232:233], s[70:71], 0, v[144:145]
	s_add_i32 m0, s69, 0x2000
	s_nop 0
	global_load_lds_dwordx4 v[232:233], off
	v_lshl_add_u64 v[232:233], s[4:5], 0, v[34:35]
	s_mov_b32 m0, s50
	s_nop 0
	global_load_lds_dwordx4 v[232:233], off
	s_mov_b32 m0, s51
	s_nop 0
	global_load_lds_dwordx4 v[242:243], off
	ds_read_b128 v[178:181], v164 offset:16384
	ds_read_b128 v[182:185], v164 offset:17408
	ds_read_b128 v[186:189], v164 offset:18432
	ds_read_b128 v[190:193], v164 offset:19456
	ds_read_b128 v[194:197], v164 offset:20480
	ds_read_b128 v[224:227], v164 offset:21504
	ds_read_b128 v[228:231], v164 offset:22528
	ds_read_b128 v[238:241], v164 offset:23552
	s_waitcnt vmcnt(8)
	s_waitcnt lgkmcnt(0)
	s_barrier
	s_waitcnt lgkmcnt(0)
	v_mfma_f32_16x16x32_bf16 v[64:67], v[132:135], v[178:181], v[64:67]
	v_mfma_f32_16x16x32_bf16 v[60:63], v[140:143], v[178:181], v[60:63]
	v_mfma_f32_16x16x32_bf16 v[56:59], v[132:135], v[186:189], v[56:59]
	v_mfma_f32_16x16x32_bf16 v[44:47], v[140:143], v[186:189], v[44:47]
	v_mfma_f32_16x16x32_bf16 v[40:43], v[132:135], v[194:197], v[40:43]
	v_mfma_f32_16x16x32_bf16 v[26:29], v[140:143], v[194:197], v[26:29]
	v_mfma_f32_16x16x32_bf16 v[22:25], v[132:135], v[228:231], v[22:25]
	v_mfma_f32_16x16x32_bf16 v[10:13], v[140:143], v[228:231], v[10:13]
	v_mfma_f32_16x16x32_bf16 v[64:67], v[136:139], v[182:185], v[64:67]
	v_mfma_f32_16x16x32_bf16 v[60:63], v[154:157], v[182:185], v[60:63]
	v_mfma_f32_16x16x32_bf16 v[56:59], v[136:139], v[190:193], v[56:59]
	v_mfma_f32_16x16x32_bf16 v[44:47], v[154:157], v[190:193], v[44:47]
	v_mfma_f32_16x16x32_bf16 v[40:43], v[136:139], v[224:227], v[40:43]
	v_mfma_f32_16x16x32_bf16 v[26:29], v[154:157], v[224:227], v[26:29]
	v_mfma_f32_16x16x32_bf16 v[22:25], v[136:139], v[238:241], v[22:25]
	v_mfma_f32_16x16x32_bf16 v[10:13], v[154:157], v[238:241], v[10:13]
	v_mfma_f32_16x16x32_bf16 v[52:55], v[158:161], v[178:181], v[52:55]
	v_mfma_f32_16x16x32_bf16 v[48:51], v[170:173], v[178:181], v[48:51]
	v_mfma_f32_16x16x32_bf16 v[36:39], v[158:161], v[186:189], v[36:39]
	v_mfma_f32_16x16x32_bf16 v[30:33], v[170:173], v[186:189], v[30:33]
	v_mfma_f32_16x16x32_bf16 v[18:21], v[158:161], v[194:197], v[18:21]
	v_mfma_f32_16x16x32_bf16 v[14:17], v[170:173], v[194:197], v[14:17]
	v_mfma_f32_16x16x32_bf16 v[6:9], v[158:161], v[228:231], v[6:9]
	v_mfma_f32_16x16x32_bf16 v[2:5], v[170:173], v[228:231], v[2:5]
	v_mfma_f32_16x16x32_bf16 v[52:55], v[166:169], v[182:185], v[52:55]
	v_mfma_f32_16x16x32_bf16 v[48:51], v[174:177], v[182:185], v[48:51]
	v_mfma_f32_16x16x32_bf16 v[36:39], v[166:169], v[190:193], v[36:39]
	v_mfma_f32_16x16x32_bf16 v[30:33], v[174:177], v[190:193], v[30:33]
	v_mfma_f32_16x16x32_bf16 v[18:21], v[166:169], v[224:227], v[18:21]
	v_mfma_f32_16x16x32_bf16 v[14:17], v[174:177], v[224:227], v[14:17]
	v_mfma_f32_16x16x32_bf16 v[6:9], v[166:169], v[238:241], v[6:9]
	v_mfma_f32_16x16x32_bf16 v[2:5], v[174:177], v[238:241], v[2:5]
	s_barrier
	s_add_i32 s69, 0, 0x18000
	s_add_i32 s70, 0, 0x1c000
	s_mov_b32 m0, s52
	v_lshl_add_u64 v[244:245], s[4:5], 0, v[148:149]
	global_load_lds_dwordx4 v[244:245], off
	v_lshl_add_u64 v[244:245], s[4:5], 0, v[146:147]
	s_mov_b32 m0, s53
	s_nop 0
	global_load_lds_dwordx4 v[244:245], off
	v_add_u32_e32 v154, s69, v162
	v_add_u32_e32 v165, s70, v162
	ds_read_b128 v[132:135], v154
	ds_read_b128 v[136:139], v154 offset:1024
	ds_read_b128 v[140:143], v154 offset:2048
	ds_read_b128 v[154:157], v154 offset:3072
	ds_read_b128 v[158:161], v165
	ds_read_b128 v[166:169], v165 offset:1024
	ds_read_b128 v[170:173], v165 offset:2048
	ds_read_b128 v[174:177], v165 offset:3072
	ds_read_b128 v[178:181], v164 offset:32768
	ds_read_b128 v[182:185], v164 offset:33792
	ds_read_b128 v[186:189], v164 offset:34816
	ds_read_b128 v[190:193], v164 offset:35840
	ds_read_b128 v[194:197], v164 offset:36864
	ds_read_b128 v[224:227], v164 offset:37888
	ds_read_b128 v[228:231], v164 offset:38912
	ds_read_b128 v[238:241], v164 offset:39936
	s_waitcnt vmcnt(8)
	s_waitcnt lgkmcnt(0)
	s_barrier
	s_waitcnt lgkmcnt(0)
	v_mfma_f32_16x16x32_bf16 v[128:131], v[132:135], v[178:181], v[128:131]
	v_mfma_f32_16x16x32_bf16 v[124:127], v[140:143], v[178:181], v[124:127]
	v_mfma_f32_16x16x32_bf16 v[120:123], v[132:135], v[186:189], v[120:123]
	v_mfma_f32_16x16x32_bf16 v[108:111], v[140:143], v[186:189], v[108:111]
	v_mfma_f32_16x16x32_bf16 v[104:107], v[132:135], v[194:197], v[104:107]
	v_mfma_f32_16x16x32_bf16 v[92:95], v[140:143], v[194:197], v[92:95]
	v_mfma_f32_16x16x32_bf16 v[88:91], v[132:135], v[228:231], v[88:91]
	v_mfma_f32_16x16x32_bf16 v[76:79], v[140:143], v[228:231], v[76:79]
	v_mfma_f32_16x16x32_bf16 v[128:131], v[136:139], v[182:185], v[128:131]
	v_mfma_f32_16x16x32_bf16 v[124:127], v[154:157], v[182:185], v[124:127]
	v_mfma_f32_16x16x32_bf16 v[120:123], v[136:139], v[190:193], v[120:123]
	v_mfma_f32_16x16x32_bf16 v[108:111], v[154:157], v[190:193], v[108:111]
	v_mfma_f32_16x16x32_bf16 v[104:107], v[136:139], v[224:227], v[104:107]
	v_mfma_f32_16x16x32_bf16 v[92:95], v[154:157], v[224:227], v[92:95]
	v_mfma_f32_16x16x32_bf16 v[88:91], v[136:139], v[238:241], v[88:91]
	v_mfma_f32_16x16x32_bf16 v[76:79], v[154:157], v[238:241], v[76:79]
	v_mfma_f32_16x16x32_bf16 v[116:119], v[158:161], v[178:181], v[116:119]
	v_mfma_f32_16x16x32_bf16 v[112:115], v[170:173], v[178:181], v[112:115]
	v_mfma_f32_16x16x32_bf16 v[100:103], v[158:161], v[186:189], v[100:103]
	v_mfma_f32_16x16x32_bf16 v[96:99], v[170:173], v[186:189], v[96:99]
	v_mfma_f32_16x16x32_bf16 v[84:87], v[158:161], v[194:197], v[84:87]
	v_mfma_f32_16x16x32_bf16 v[80:83], v[170:173], v[194:197], v[80:83]
	v_mfma_f32_16x16x32_bf16 v[72:75], v[158:161], v[228:231], v[72:75]
	v_mfma_f32_16x16x32_bf16 v[68:71], v[170:173], v[228:231], v[68:71]
	v_mfma_f32_16x16x32_bf16 v[116:119], v[166:169], v[182:185], v[116:119]
	v_mfma_f32_16x16x32_bf16 v[112:115], v[174:177], v[182:185], v[112:115]
	v_mfma_f32_16x16x32_bf16 v[100:103], v[166:169], v[190:193], v[100:103]
	v_mfma_f32_16x16x32_bf16 v[96:99], v[174:177], v[190:193], v[96:99]
	v_mfma_f32_16x16x32_bf16 v[84:87], v[166:169], v[224:227], v[84:87]
	v_mfma_f32_16x16x32_bf16 v[80:83], v[174:177], v[224:227], v[80:83]
	v_mfma_f32_16x16x32_bf16 v[72:75], v[166:169], v[238:241], v[72:75]
	v_mfma_f32_16x16x32_bf16 v[68:71], v[174:177], v[238:241], v[68:71]
	s_barrier
	s_add_i32 s4, s69, s49
	v_lshl_add_u64 v[198:199], v[198:199], 0, s[78:79]
	s_mov_b32 m0, s4
	s_nop 0
	global_load_lds_dwordx4 v[198:199], off
	s_add_i32 m0, s4, 0x2000
	s_add_u32 s4, s44, 0x80080
	v_lshl_add_u64 v[198:199], v[212:213], 0, s[78:79]
	s_addc_u32 s5, s45, 0
	s_add_i32 s44, s70, s49
	global_load_lds_dwordx4 v[198:199], off
	v_lshl_add_u64 v[198:199], s[4:5], 0, v[34:35]
	s_mov_b32 m0, s44
	s_nop 0
	global_load_lds_dwordx4 v[198:199], off
	v_lshl_add_u64 v[198:199], s[4:5], 0, v[144:145]
	s_add_i32 m0, s44, 0x2000
	s_nop 0
	global_load_lds_dwordx4 v[198:199], off
	v_lshl_add_u64 v[198:199], v[232:233], 0, s[78:79]
	s_mov_b32 m0, s54
	s_nop 0
	global_load_lds_dwordx4 v[198:199], off
	v_lshl_add_u64 v[198:199], v[242:243], 0, s[78:79]
	s_mov_b32 m0, s55
	s_nop 0
	global_load_lds_dwordx4 v[198:199], off
	ds_read_b128 v[178:181], v164 offset:49152
	ds_read_b128 v[182:185], v164 offset:50176
	ds_read_b128 v[186:189], v164 offset:51200
	ds_read_b128 v[190:193], v164 offset:52224
	ds_read_b128 v[194:197], v164 offset:53248
	ds_read_b128 v[224:227], v164 offset:54272
	ds_read_b128 v[228:231], v164 offset:55296
	ds_read_b128 v[238:241], v164 offset:56320
	s_waitcnt vmcnt(8)
	s_waitcnt lgkmcnt(0)
	s_barrier
	s_waitcnt lgkmcnt(0)
	v_mfma_f32_16x16x32_bf16 v[64:67], v[132:135], v[178:181], v[64:67]
	v_mfma_f32_16x16x32_bf16 v[60:63], v[140:143], v[178:181], v[60:63]
	v_mfma_f32_16x16x32_bf16 v[56:59], v[132:135], v[186:189], v[56:59]
	v_mfma_f32_16x16x32_bf16 v[44:47], v[140:143], v[186:189], v[44:47]
	v_mfma_f32_16x16x32_bf16 v[40:43], v[132:135], v[194:197], v[40:43]
	v_mfma_f32_16x16x32_bf16 v[26:29], v[140:143], v[194:197], v[26:29]
	v_mfma_f32_16x16x32_bf16 v[22:25], v[132:135], v[228:231], v[22:25]
	v_mfma_f32_16x16x32_bf16 v[10:13], v[140:143], v[228:231], v[10:13]
	v_mfma_f32_16x16x32_bf16 v[64:67], v[136:139], v[182:185], v[64:67]
	v_mfma_f32_16x16x32_bf16 v[60:63], v[154:157], v[182:185], v[60:63]
	v_mfma_f32_16x16x32_bf16 v[56:59], v[136:139], v[190:193], v[56:59]
	v_mfma_f32_16x16x32_bf16 v[44:47], v[154:157], v[190:193], v[44:47]
	v_mfma_f32_16x16x32_bf16 v[40:43], v[136:139], v[224:227], v[40:43]
	v_mfma_f32_16x16x32_bf16 v[26:29], v[154:157], v[224:227], v[26:29]
	v_mfma_f32_16x16x32_bf16 v[22:25], v[136:139], v[238:241], v[22:25]
	v_mfma_f32_16x16x32_bf16 v[10:13], v[154:157], v[238:241], v[10:13]
	v_mfma_f32_16x16x32_bf16 v[52:55], v[158:161], v[178:181], v[52:55]
	v_mfma_f32_16x16x32_bf16 v[48:51], v[170:173], v[178:181], v[48:51]
	v_mfma_f32_16x16x32_bf16 v[36:39], v[158:161], v[186:189], v[36:39]
	v_mfma_f32_16x16x32_bf16 v[30:33], v[170:173], v[186:189], v[30:33]
	v_mfma_f32_16x16x32_bf16 v[18:21], v[158:161], v[194:197], v[18:21]
	v_mfma_f32_16x16x32_bf16 v[14:17], v[170:173], v[194:197], v[14:17]
	v_mfma_f32_16x16x32_bf16 v[6:9], v[158:161], v[228:231], v[6:9]
	v_mfma_f32_16x16x32_bf16 v[2:5], v[170:173], v[228:231], v[2:5]
	v_mfma_f32_16x16x32_bf16 v[52:55], v[166:169], v[182:185], v[52:55]
	v_mfma_f32_16x16x32_bf16 v[48:51], v[174:177], v[182:185], v[48:51]
	v_mfma_f32_16x16x32_bf16 v[36:39], v[166:169], v[190:193], v[36:39]
	v_mfma_f32_16x16x32_bf16 v[30:33], v[174:177], v[190:193], v[30:33]
	v_mfma_f32_16x16x32_bf16 v[18:21], v[166:169], v[224:227], v[18:21]
	v_mfma_f32_16x16x32_bf16 v[14:17], v[174:177], v[224:227], v[14:17]
	v_mfma_f32_16x16x32_bf16 v[6:9], v[166:169], v[238:241], v[6:9]
	v_mfma_f32_16x16x32_bf16 v[2:5], v[174:177], v[238:241], v[2:5]
	s_barrier
	s_add_i32 s68, s68, 2
	s_add_u32 s29, s29, 0x100
	s_addc_u32 s31, s31, 0
	s_add_u32 s38, s38, 0x100
	s_addc_u32 s39, s39, 0
	s_cmp_gt_u32 s68, 29
	s_cbranch_scc0 .LBB0_787
	s_setprio 0
	s_and_b64 vcc, exec, s[26:27]
	s_cbranch_vccz .LBB0_790
	s_barrier

.Lsp1199:
.LBB0_1199:
	s_add_u32 s4, s34, 0x80
	s_addc_u32 s5, s35, 0
	s_add_i32 s53, 0, 0x10000
	s_cmp_eq_u32 s52, 4
	s_cselect_b32 s5, s27, s5
	s_cselect_b32 s4, s26, s4
	s_cselect_b32 s37, s29, s51
	s_cselect_b32 s36, s28, s50
	s_add_i32 s56, 0, 0x14000
	v_lshl_add_u64 v[148:149], s[34:35], 0, v[146:147]
	s_add_i32 m0, s41, 0xc000
	s_nop 0
	global_load_lds_dwordx4 v[148:149], off
	v_lshl_add_u64 v[148:149], s[34:35], 0, v[144:145]
	s_add_i32 m0, s41, 0xe000
	s_nop 0
	global_load_lds_dwordx4 v[148:149], off
	v_add_u32_e32 v34, s53, v1
	ds_read_b128 v[154:157], v34
	ds_read_b128 v[158:161], v34 offset:1024
	ds_read_b128 v[162:165], v34 offset:2048
	ds_read_b128 v[166:169], v34 offset:3072
	v_add_u32_e32 v34, s56, v1
	ds_read_b128 v[170:173], v34
	ds_read_b128 v[174:177], v34 offset:1024
	ds_read_b128 v[178:181], v34 offset:2048
	ds_read_b128 v[182:185], v34 offset:3072
	ds_read_b128 v[186:189], v152
	ds_read_b128 v[190:193], v152 offset:1024
	ds_read_b128 v[194:197], v152 offset:2048
	ds_read_b128 v[224:227], v152 offset:3072
	ds_read_b128 v[228:231], v152 offset:4096
	ds_read_b128 v[238:241], v152 offset:5120
	ds_read_b128 v[242:245], v152 offset:6144
	ds_read_b128 v[246:249], v152 offset:7168
	s_waitcnt vmcnt(8)
	s_waitcnt lgkmcnt(0)
	s_barrier
	s_waitcnt lgkmcnt(0)
	v_mfma_f32_16x16x32_bf16 v[128:131], v[154:157], v[186:189], v[128:131]
	v_mfma_f32_16x16x32_bf16 v[124:127], v[162:165], v[186:189], v[124:127]
	v_mfma_f32_16x16x32_bf16 v[116:119], v[154:157], v[194:197], v[116:119]
	v_mfma_f32_16x16x32_bf16 v[108:111], v[162:165], v[194:197], v[108:111]
	v_mfma_f32_16x16x32_bf16 v[100:103], v[154:157], v[228:231], v[100:103]
	v_mfma_f32_16x16x32_bf16 v[92:95], v[162:165], v[228:231], v[92:95]
	v_mfma_f32_16x16x32_bf16 v[84:87], v[154:157], v[242:245], v[84:87]
	v_mfma_f32_16x16x32_bf16 v[76:79], v[162:165], v[242:245], v[76:79]
	v_mfma_f32_16x16x32_bf16 v[128:131], v[158:161], v[190:193], v[128:131]
	v_mfma_f32_16x16x32_bf16 v[124:127], v[166:169], v[190:193], v[124:127]
	v_mfma_f32_16x16x32_bf16 v[116:119], v[158:161], v[224:227], v[116:119]
	v_mfma_f32_16x16x32_bf16 v[108:111], v[166:169], v[224:227], v[108:111]
	v_mfma_f32_16x16x32_bf16 v[100:103], v[158:161], v[238:241], v[100:103]
	v_mfma_f32_16x16x32_bf16 v[92:95], v[166:169], v[238:241], v[92:95]
	v_mfma_f32_16x16x32_bf16 v[84:87], v[158:161], v[246:249], v[84:87]
	v_mfma_f32_16x16x32_bf16 v[76:79], v[166:169], v[246:249], v[76:79]
	v_mfma_f32_16x16x32_bf16 v[120:123], v[170:173], v[186:189], v[120:123]
	v_mfma_f32_16x16x32_bf16 v[112:115], v[178:181], v[186:189], v[112:115]
	v_mfma_f32_16x16x32_bf16 v[104:107], v[170:173], v[194:197], v[104:107]
	v_mfma_f32_16x16x32_bf16 v[96:99], v[178:181], v[194:197], v[96:99]
	v_mfma_f32_16x16x32_bf16 v[88:91], v[170:173], v[228:231], v[88:91]
	v_mfma_f32_16x16x32_bf16 v[80:83], v[178:181], v[228:231], v[80:83]
	v_mfma_f32_16x16x32_bf16 v[72:75], v[170:173], v[242:245], v[72:75]
	v_mfma_f32_16x16x32_bf16 v[68:71], v[178:181], v[242:245], v[68:71]
	v_mfma_f32_16x16x32_bf16 v[120:123], v[174:177], v[190:193], v[120:123]
	v_mfma_f32_16x16x32_bf16 v[112:115], v[182:185], v[190:193], v[112:115]
	v_mfma_f32_16x16x32_bf16 v[104:107], v[174:177], v[224:227], v[104:107]
	v_mfma_f32_16x16x32_bf16 v[96:99], v[182:185], v[224:227], v[96:99]
	v_mfma_f32_16x16x32_bf16 v[88:91], v[174:177], v[238:241], v[88:91]
	v_mfma_f32_16x16x32_bf16 v[80:83], v[182:185], v[238:241], v[80:83]
	v_mfma_f32_16x16x32_bf16 v[72:75], v[174:177], v[246:249], v[72:75]
	v_mfma_f32_16x16x32_bf16 v[68:71], v[182:185], v[246:249], v[68:71]
	s_barrier
	s_add_i32 s53, s53, s14
	v_lshl_add_u64 v[148:149], s[36:37], 0, v[138:139]
	s_mov_b32 m0, s53
	s_nop 0
	global_load_lds_dwordx4 v[148:149], off
	s_add_i32 m0, s53, 0x2000
	s_add_u32 s54, s36, 0x20000
	v_lshl_add_u64 v[198:199], s[36:37], 0, v[132:133]
	s_addc_u32 s55, s37, 0
	s_add_i32 s53, s56, s14
	global_load_lds_dwordx4 v[198:199], off
	v_lshl_add_u64 v[208:209], s[54:55], 0, v[138:139]
	s_mov_b32 m0, s53
	v_lshl_add_u64 v[212:213], s[4:5], 0, v[134:135]
	global_load_lds_dwordx4 v[208:209], off
	v_lshl_add_u64 v[208:209], s[54:55], 0, v[132:133]
	s_add_i32 m0, s53, 0x2000
	s_nop 0
	global_load_lds_dwordx4 v[208:209], off
	v_lshl_add_u64 v[208:209], s[4:5], 0, v[140:141]
	s_mov_b32 m0, s41
	s_nop 0
	global_load_lds_dwordx4 v[208:209], off
	s_mov_b32 m0, s42
	s_nop 0
	global_load_lds_dwordx4 v[212:213], off
	ds_read_b128 v[186:189], v152 offset:16384
	ds_read_b128 v[190:193], v152 offset:17408
	ds_read_b128 v[194:197], v152 offset:18432
	ds_read_b128 v[224:227], v152 offset:19456
	ds_read_b128 v[228:231], v152 offset:20480
	ds_read_b128 v[238:241], v152 offset:21504
	ds_read_b128 v[242:245], v152 offset:22528
	ds_read_b128 v[246:249], v152 offset:23552
	s_waitcnt vmcnt(8)
	s_waitcnt lgkmcnt(0)
	s_barrier
	s_waitcnt lgkmcnt(0)
	v_mfma_f32_16x16x32_bf16 v[64:67], v[154:157], v[186:189], v[64:67]
	v_mfma_f32_16x16x32_bf16 v[60:63], v[162:165], v[186:189], v[60:63]
	v_mfma_f32_16x16x32_bf16 v[52:55], v[154:157], v[194:197], v[52:55]
	v_mfma_f32_16x16x32_bf16 v[44:47], v[162:165], v[194:197], v[44:47]
	v_mfma_f32_16x16x32_bf16 v[36:39], v[154:157], v[228:231], v[36:39]
	v_mfma_f32_16x16x32_bf16 v[26:29], v[162:165], v[228:231], v[26:29]
	v_mfma_f32_16x16x32_bf16 v[18:21], v[154:157], v[242:245], v[18:21]
	v_mfma_f32_16x16x32_bf16 v[10:13], v[162:165], v[242:245], v[10:13]
	v_mfma_f32_16x16x32_bf16 v[64:67], v[158:161], v[190:193], v[64:67]
	v_mfma_f32_16x16x32_bf16 v[60:63], v[166:169], v[190:193], v[60:63]
	v_mfma_f32_16x16x32_bf16 v[52:55], v[158:161], v[224:227], v[52:55]
	v_mfma_f32_16x16x32_bf16 v[44:47], v[166:169], v[224:227], v[44:47]
	v_mfma_f32_16x16x32_bf16 v[36:39], v[158:161], v[238:241], v[36:39]
	v_mfma_f32_16x16x32_bf16 v[26:29], v[166:169], v[238:241], v[26:29]
	v_mfma_f32_16x16x32_bf16 v[18:21], v[158:161], v[246:249], v[18:21]
	v_mfma_f32_16x16x32_bf16 v[10:13], v[166:169], v[246:249], v[10:13]
	v_mfma_f32_16x16x32_bf16 v[56:59], v[170:173], v[186:189], v[56:59]
	v_mfma_f32_16x16x32_bf16 v[48:51], v[178:181], v[186:189], v[48:51]
	v_mfma_f32_16x16x32_bf16 v[40:43], v[170:173], v[194:197], v[40:43]
	v_mfma_f32_16x16x32_bf16 v[30:33], v[178:181], v[194:197], v[30:33]
	v_mfma_f32_16x16x32_bf16 v[22:25], v[170:173], v[228:231], v[22:25]
	v_mfma_f32_16x16x32_bf16 v[14:17], v[178:181], v[228:231], v[14:17]
	v_mfma_f32_16x16x32_bf16 v[6:9], v[170:173], v[242:245], v[6:9]
	v_mfma_f32_16x16x32_bf16 v[2:5], v[178:181], v[242:245], v[2:5]
	v_mfma_f32_16x16x32_bf16 v[56:59], v[174:177], v[190:193], v[56:59]
	v_mfma_f32_16x16x32_bf16 v[48:51], v[182:185], v[190:193], v[48:51]
	v_mfma_f32_16x16x32_bf16 v[40:43], v[174:177], v[224:227], v[40:43]
	v_mfma_f32_16x16x32_bf16 v[30:33], v[182:185], v[224:227], v[30:33]
	v_mfma_f32_16x16x32_bf16 v[22:25], v[174:177], v[238:241], v[22:25]
	v_mfma_f32_16x16x32_bf16 v[14:17], v[182:185], v[238:241], v[14:17]
	v_mfma_f32_16x16x32_bf16 v[6:9], v[174:177], v[246:249], v[6:9]
	v_mfma_f32_16x16x32_bf16 v[2:5], v[182:185], v[246:249], v[2:5]
	s_barrier
	s_add_i32 s53, 0, 0x18000
	s_add_i32 s54, 0, 0x1c000
	s_mov_b32 m0, s43
	v_lshl_add_u64 v[232:233], s[4:5], 0, v[142:143]
	global_load_lds_dwordx4 v[232:233], off
	v_lshl_add_u64 v[232:233], s[4:5], 0, v[136:137]
	s_mov_b32 m0, s44
	s_nop 0
	global_load_lds_dwordx4 v[232:233], off
	v_add_u32_e32 v34, s53, v1
	ds_read_b128 v[154:157], v34
	ds_read_b128 v[158:161], v34 offset:1024
	ds_read_b128 v[162:165], v34 offset:2048
	ds_read_b128 v[166:169], v34 offset:3072
	v_add_u32_e32 v34, s54, v1
	ds_read_b128 v[170:173], v34
	ds_read_b128 v[174:177], v34 offset:1024
	ds_read_b128 v[178:181], v34 offset:2048
	ds_read_b128 v[182:185], v34 offset:3072
	ds_read_b128 v[186:189], v152 offset:32768
	ds_read_b128 v[190:193], v152 offset:33792
	ds_read_b128 v[194:197], v152 offset:34816
	ds_read_b128 v[224:227], v152 offset:35840
	ds_read_b128 v[228:231], v152 offset:36864
	ds_read_b128 v[238:241], v152 offset:37888
	ds_read_b128 v[242:245], v152 offset:38912
	ds_read_b128 v[246:249], v152 offset:39936
	s_waitcnt vmcnt(8)
	s_waitcnt lgkmcnt(0)
	s_barrier
	s_waitcnt lgkmcnt(0)
	v_mfma_f32_16x16x32_bf16 v[128:131], v[154:157], v[186:189], v[128:131]
	v_mfma_f32_16x16x32_bf16 v[124:127], v[162:165], v[186:189], v[124:127]
	v_mfma_f32_16x16x32_bf16 v[116:119], v[154:157], v[194:197], v[116:119]
	v_mfma_f32_16x16x32_bf16 v[108:111], v[162:165], v[194:197], v[108:111]
	v_mfma_f32_16x16x32_bf16 v[100:103], v[154:157], v[228:231], v[100:103]
	v_mfma_f32_16x16x32_bf16 v[92:95], v[162:165], v[228:231], v[92:95]
	v_mfma_f32_16x16x32_bf16 v[84:87], v[154:157], v[242:245], v[84:87]
	v_mfma_f32_16x16x32_bf16 v[76:79], v[162:165], v[242:245], v[76:79]
	v_mfma_f32_16x16x32_bf16 v[128:131], v[158:161], v[190:193], v[128:131]
	v_mfma_f32_16x16x32_bf16 v[124:127], v[166:169], v[190:193], v[124:127]
	v_mfma_f32_16x16x32_bf16 v[116:119], v[158:161], v[224:227], v[116:119]
	v_mfma_f32_16x16x32_bf16 v[108:111], v[166:169], v[224:227], v[108:111]
	v_mfma_f32_16x16x32_bf16 v[100:103], v[158:161], v[238:241], v[100:103]
	v_mfma_f32_16x16x32_bf16 v[92:95], v[166:169], v[238:241], v[92:95]
	v_mfma_f32_16x16x32_bf16 v[84:87], v[158:161], v[246:249], v[84:87]
	v_mfma_f32_16x16x32_bf16 v[76:79], v[166:169], v[246:249], v[76:79]
	v_mfma_f32_16x16x32_bf16 v[120:123], v[170:173], v[186:189], v[120:123]
	v_mfma_f32_16x16x32_bf16 v[112:115], v[178:181], v[186:189], v[112:115]
	v_mfma_f32_16x16x32_bf16 v[104:107], v[170:173], v[194:197], v[104:107]
	v_mfma_f32_16x16x32_bf16 v[96:99], v[178:181], v[194:197], v[96:99]
	v_mfma_f32_16x16x32_bf16 v[88:91], v[170:173], v[228:231], v[88:91]
	v_mfma_f32_16x16x32_bf16 v[80:83], v[178:181], v[228:231], v[80:83]
	v_mfma_f32_16x16x32_bf16 v[72:75], v[170:173], v[242:245], v[72:75]
	v_mfma_f32_16x16x32_bf16 v[68:71], v[178:181], v[242:245], v[68:71]
	v_mfma_f32_16x16x32_bf16 v[120:123], v[174:177], v[190:193], v[120:123]
	v_mfma_f32_16x16x32_bf16 v[112:115], v[182:185], v[190:193], v[112:115]
	v_mfma_f32_16x16x32_bf16 v[104:107], v[174:177], v[224:227], v[104:107]
	v_mfma_f32_16x16x32_bf16 v[96:99], v[182:185], v[224:227], v[96:99]
	v_mfma_f32_16x16x32_bf16 v[88:91], v[174:177], v[238:241], v[88:91]
	v_mfma_f32_16x16x32_bf16 v[80:83], v[182:185], v[238:241], v[80:83]
	v_mfma_f32_16x16x32_bf16 v[72:75], v[174:177], v[246:249], v[72:75]
	v_mfma_f32_16x16x32_bf16 v[68:71], v[182:185], v[246:249], v[68:71]
	s_barrier
	s_add_i32 s4, s53, s14
	v_lshl_add_u64 v[148:149], v[148:149], 0, s[78:79]
	s_mov_b32 m0, s4
	s_nop 0
	global_load_lds_dwordx4 v[148:149], off
	s_add_i32 m0, s4, 0x2000
	s_add_u32 s4, s36, 0x20080
	v_lshl_add_u64 v[148:149], v[198:199], 0, s[78:79]
	s_addc_u32 s5, s37, 0
	s_add_i32 s36, s54, s14
	global_load_lds_dwordx4 v[148:149], off
	v_lshl_add_u64 v[148:149], s[4:5], 0, v[138:139]
	s_mov_b32 m0, s36
	s_nop 0
	global_load_lds_dwordx4 v[148:149], off
	v_lshl_add_u64 v[148:149], s[4:5], 0, v[132:133]
	s_add_i32 m0, s36, 0x2000
	s_nop 0
	global_load_lds_dwordx4 v[148:149], off
	v_lshl_add_u64 v[148:149], v[208:209], 0, s[78:79]
	s_mov_b32 m0, s45
	s_nop 0
	global_load_lds_dwordx4 v[148:149], off
	v_lshl_add_u64 v[148:149], v[212:213], 0, s[78:79]
	s_mov_b32 m0, s46
	s_nop 0
	global_load_lds_dwordx4 v[148:149], off
	ds_read_b128 v[186:189], v152 offset:49152
	ds_read_b128 v[190:193], v152 offset:50176
	ds_read_b128 v[194:197], v152 offset:51200
	ds_read_b128 v[224:227], v152 offset:52224
	ds_read_b128 v[228:231], v152 offset:53248
	ds_read_b128 v[238:241], v152 offset:54272
	ds_read_b128 v[242:245], v152 offset:55296
	ds_read_b128 v[246:249], v152 offset:56320
	s_waitcnt vmcnt(8)
	s_waitcnt lgkmcnt(0)
	s_barrier
	s_waitcnt lgkmcnt(0)
	v_mfma_f32_16x16x32_bf16 v[64:67], v[154:157], v[186:189], v[64:67]
	v_mfma_f32_16x16x32_bf16 v[60:63], v[162:165], v[186:189], v[60:63]
	v_mfma_f32_16x16x32_bf16 v[52:55], v[154:157], v[194:197], v[52:55]
	v_mfma_f32_16x16x32_bf16 v[44:47], v[162:165], v[194:197], v[44:47]
	v_mfma_f32_16x16x32_bf16 v[36:39], v[154:157], v[228:231], v[36:39]
	v_mfma_f32_16x16x32_bf16 v[26:29], v[162:165], v[228:231], v[26:29]
	v_mfma_f32_16x16x32_bf16 v[18:21], v[154:157], v[242:245], v[18:21]
	v_mfma_f32_16x16x32_bf16 v[10:13], v[162:165], v[242:245], v[10:13]
	v_mfma_f32_16x16x32_bf16 v[64:67], v[158:161], v[190:193], v[64:67]
	v_mfma_f32_16x16x32_bf16 v[60:63], v[166:169], v[190:193], v[60:63]
	v_mfma_f32_16x16x32_bf16 v[52:55], v[158:161], v[224:227], v[52:55]
	v_mfma_f32_16x16x32_bf16 v[44:47], v[166:169], v[224:227], v[44:47]
	v_mfma_f32_16x16x32_bf16 v[36:39], v[158:161], v[238:241], v[36:39]
	v_mfma_f32_16x16x32_bf16 v[26:29], v[166:169], v[238:241], v[26:29]
	v_mfma_f32_16x16x32_bf16 v[18:21], v[158:161], v[246:249], v[18:21]
	v_mfma_f32_16x16x32_bf16 v[10:13], v[166:169], v[246:249], v[10:13]
	v_mfma_f32_16x16x32_bf16 v[56:59], v[170:173], v[186:189], v[56:59]
	v_mfma_f32_16x16x32_bf16 v[48:51], v[178:181], v[186:189], v[48:51]
	v_mfma_f32_16x16x32_bf16 v[40:43], v[170:173], v[194:197], v[40:43]
	v_mfma_f32_16x16x32_bf16 v[30:33], v[178:181], v[194:197], v[30:33]
	v_mfma_f32_16x16x32_bf16 v[22:25], v[170:173], v[228:231], v[22:25]
	v_mfma_f32_16x16x32_bf16 v[14:17], v[178:181], v[228:231], v[14:17]
	v_mfma_f32_16x16x32_bf16 v[6:9], v[170:173], v[242:245], v[6:9]
	v_mfma_f32_16x16x32_bf16 v[2:5], v[178:181], v[242:245], v[2:5]
	v_mfma_f32_16x16x32_bf16 v[56:59], v[174:177], v[190:193], v[56:59]
	v_mfma_f32_16x16x32_bf16 v[48:51], v[182:185], v[190:193], v[48:51]
	v_mfma_f32_16x16x32_bf16 v[40:43], v[174:177], v[224:227], v[40:43]
	v_mfma_f32_16x16x32_bf16 v[30:33], v[182:185], v[224:227], v[30:33]
	v_mfma_f32_16x16x32_bf16 v[22:25], v[174:177], v[238:241], v[22:25]
	v_mfma_f32_16x16x32_bf16 v[14:17], v[182:185], v[238:241], v[14:17]
	v_mfma_f32_16x16x32_bf16 v[6:9], v[174:177], v[246:249], v[6:9]
	v_mfma_f32_16x16x32_bf16 v[2:5], v[182:185], v[246:249], v[2:5]
	s_barrier
	s_add_i32 s52, s52, 2
	s_add_u32 s50, s50, 0x100
	s_addc_u32 s51, s51, 0
	s_add_u32 s34, s34, 0x100
	s_addc_u32 s35, s35, 0
	s_cmp_gt_u32 s52, 5
	s_cbranch_scc0 .LBB0_1199
	s_setprio 0
	s_and_b64 vcc, exec, s[22:23]
	s_cbranch_vccz .LBB0_1202
	s_barrier
